# non-temporal also on the transposed-weight stores and norm1's expert-row gathers
# speedup vs baseline: 1.0209x; 1.0025x over previous
.LBB0_40:
	s_mul_hi_i32 s8, s83, 0x4fec04ff
	s_lshr_b32 s12, s8, 31
	s_ashr_i32 s8, s8, 13
	s_add_i32 s12, s8, s12
	s_mul_i32 s8, s12, 0xffff9980
	s_add_i32 s90, s83, s8
	s_ashr_i32 s13, s12, 31
	s_mul_i32 s14, s12, 0x1300000
	s_mul_hi_i32 s8, s12, 0x1300000
	s_waitcnt lgkmcnt(0)
	s_add_u32 s88, s10, s14
	s_addc_u32 s89, s11, s8
	s_cmpk_gt_i32 s90, 0xbf
	s_mov_b64 s[14:15], -1
	s_cbranch_scc0 .LBB0_62
	s_cmpk_gt_u32 s90, 0x3bf
	s_cbranch_scc0 .LBB0_59
	s_cmpk_gt_u32 s90, 0x47f
	s_cbranch_scc0 .LBB0_56
	s_cmpk_gt_u32 s90, 0x57f
	s_cbranch_scc0 .LBB0_53
	s_cmpk_gt_u32 s90, 0x67f
	s_cbranch_scc0 .LBB0_50
	s_cmpk_gt_u32 s90, 0x467f
	s_cbranch_scc0 .LBB0_47
	s_add_i32 s8, s90, 0xffffb980
	s_load_dwordx2 s[14:15], s[28:29], 0xc8
	s_lshr_b32 s8, s8, 9
	s_lshl_b64 s[44:45], s[12:13], 4
	s_add_u32 s44, s44, s8
	s_addc_u32 s45, s45, 0
	s_lshl_b64 s[92:93], s[44:45], 23
	s_waitcnt lgkmcnt(0)
	s_add_u32 s40, s14, s92
	s_addc_u32 s42, s15, s93
	s_lshl_b32 s8, s12, 8
	s_sub_i32 s8, s86, s8
	s_and_b32 s91, s85, 0x7c0
	s_and_b32 s8, s8, 0x3c0
	s_lshl_b64 s[14:15], s[44:45], 21
	s_add_u32 s44, s2, s14
	s_addc_u32 s45, s3, s15
	s_lshl_b32 s14, s8, 2
	s_add_u32 s14, s40, s14
	v_or_b32_e32 v52, s91, v9
	s_addc_u32 s15, s42, 0
	v_lshl_add_u64 v[10:11], s[14:15], 0, v[2:3]
	v_lshlrev_b32_e32 v52, 12, v52
	v_mov_b32_e32 v53, v3
	v_lshl_add_u64 v[10:11], v[10:11], 0, v[52:53]
	v_add_co_u32_e32 v56, vcc, s30, v10
	s_add_u32 s14, s44, s91
	s_nop 0
	v_addc_co_u32_e32 v57, vcc, 0, v11, vcc
	v_add_co_u32_e32 v60, vcc, s31, v10
	global_load_dwordx4 v[52:55], v[10:11], off nt
	s_nop 0
	global_load_dwordx4 v[56:59], v[56:57], off nt
	v_addc_co_u32_e32 v61, vcc, 0, v11, vcc
	v_add_co_u32_e32 v64, vcc, s33, v10
	s_addc_u32 s15, s45, 0
	s_nop 0
	v_addc_co_u32_e32 v65, vcc, 0, v11, vcc
	v_add_co_u32_e32 v68, vcc, s34, v10
	global_load_dwordx4 v[60:63], v[60:61], off nt
	s_nop 0
	global_load_dwordx4 v[64:67], v[64:65], off nt
	v_addc_co_u32_e32 v69, vcc, 0, v11, vcc
	v_add_co_u32_e32 v72, vcc, s35, v10
	s_nop 1
	v_addc_co_u32_e32 v73, vcc, 0, v11, vcc
	v_add_co_u32_e32 v76, vcc, s36, v10
	global_load_dwordx4 v[68:71], v[68:69], off nt
	s_nop 0
	global_load_dwordx4 v[72:75], v[72:73], off nt
	v_addc_co_u32_e32 v77, vcc, 0, v11, vcc
	v_add_co_u32_e32 v80, vcc, s37, v10
	s_nop 1
	v_addc_co_u32_e32 v81, vcc, 0, v11, vcc
	v_add_co_u32_e32 v84, vcc, s38, v10
	global_load_dwordx4 v[76:79], v[76:77], off nt
	s_nop 0
	global_load_dwordx4 v[80:83], v[80:81], off nt
	v_addc_co_u32_e32 v85, vcc, 0, v11, vcc
	v_add_co_u32_e32 v88, vcc, s39, v10
	s_nop 1
	v_addc_co_u32_e32 v89, vcc, 0, v11, vcc
	v_add_co_u32_e32 v92, vcc, s41, v10
	global_load_dwordx4 v[84:87], v[84:85], off nt
	s_nop 0
	global_load_dwordx4 v[88:91], v[88:89], off nt
	v_addc_co_u32_e32 v93, vcc, 0, v11, vcc
	v_add_co_u32_e32 v96, vcc, s43, v10
	s_nop 1
	v_addc_co_u32_e32 v97, vcc, 0, v11, vcc
	v_add_co_u32_e32 v100, vcc, s46, v10
	global_load_dwordx4 v[92:95], v[92:93], off nt
	s_nop 0
	global_load_dwordx4 v[96:99], v[96:97], off nt
	v_addc_co_u32_e32 v101, vcc, 0, v11, vcc
	v_add_co_u32_e32 v104, vcc, s47, v10
	s_nop 1
	v_addc_co_u32_e32 v105, vcc, 0, v11, vcc
	v_add_co_u32_e32 v108, vcc, s48, v10
	global_load_dwordx4 v[100:103], v[100:101], off nt
	s_nop 0
	global_load_dwordx4 v[104:107], v[104:105], off nt
	v_addc_co_u32_e32 v109, vcc, 0, v11, vcc
	v_add_co_u32_e32 v10, vcc, s49, v10
	s_nop 1
	v_addc_co_u32_e32 v11, vcc, 0, v11, vcc
	global_load_dwordx4 v[108:111], v[108:109], off nt
	s_nop 0
	global_load_dwordx4 v[112:115], v[10:11], off nt
	v_lshl_add_u64 v[10:11], s[14:15], 0, v[4:5]
	s_mov_b64 s[14:15], 0
	s_waitcnt vmcnt(14)
	ds_write2_b32 v12, v52, v56 offset1:4
	ds_write2_b32 v12, v53, v57 offset0:65 offset1:69
	ds_write2_b32 v12, v54, v58 offset0:130 offset1:134
	ds_write2_b32 v12, v55, v59 offset0:195 offset1:199
	s_waitcnt vmcnt(12)
	ds_write2_b32 v12, v60, v64 offset0:8 offset1:12
	ds_write2_b32 v12, v61, v65 offset0:73 offset1:77
	ds_write2_b32 v12, v62, v66 offset0:138 offset1:142
	ds_write2_b32 v12, v63, v67 offset0:203 offset1:207
	s_waitcnt vmcnt(10)
	ds_write2_b32 v12, v68, v72 offset0:16 offset1:20
	ds_write2_b32 v12, v69, v73 offset0:81 offset1:85
	ds_write2_b32 v12, v70, v74 offset0:146 offset1:150
	ds_write2_b32 v12, v71, v75 offset0:211 offset1:215
	s_waitcnt vmcnt(8)
	ds_write2_b32 v12, v76, v80 offset0:24 offset1:28
	ds_write2_b32 v12, v77, v81 offset0:89 offset1:93
	ds_write2_b32 v12, v78, v82 offset0:154 offset1:158
	ds_write2_b32 v12, v79, v83 offset0:219 offset1:223
	s_waitcnt vmcnt(6)
	ds_write2_b32 v12, v84, v88 offset0:32 offset1:36
	ds_write2_b32 v12, v85, v89 offset0:97 offset1:101
	ds_write2_b32 v12, v86, v90 offset0:162 offset1:166
	ds_write2_b32 v12, v87, v91 offset0:227 offset1:231
	s_waitcnt vmcnt(4)
	ds_write2_b32 v12, v92, v96 offset0:40 offset1:44
	ds_write2_b32 v12, v93, v97 offset0:105 offset1:109
	ds_write2_b32 v12, v94, v98 offset0:170 offset1:174
	ds_write2_b32 v12, v95, v99 offset0:235 offset1:239
	s_waitcnt vmcnt(2)
	ds_write2_b32 v12, v100, v104 offset0:48 offset1:52
	ds_write2_b32 v12, v101, v105 offset0:113 offset1:117
	ds_write2_b32 v12, v102, v106 offset0:178 offset1:182
	ds_write2_b32 v12, v103, v107 offset0:243 offset1:247
	s_waitcnt vmcnt(0)
	ds_write2_b32 v12, v108, v112 offset0:56 offset1:60
	ds_write2_b32 v12, v109, v113 offset0:121 offset1:125
	ds_write2_b32 v12, v110, v114 offset0:186 offset1:190
	ds_write2_b32 v12, v111, v115 offset0:251 offset1:255
	s_waitcnt lgkmcnt(0)
	ds_read2_b32 v[52:53], v14 offset1:1
	ds_read2_b32 v[54:55], v14 offset0:2 offset1:3
	ds_read2_b32 v[56:57], v14 offset0:4 offset1:5
	ds_read2_b32 v[58:59], v14 offset0:6 offset1:7
	s_waitcnt lgkmcnt(2)
	v_mul_f32_e32 v54, 0x42800000, v54
	v_mul_f32_e32 v52, 0x42800000, v52
	v_mul_f32_e32 v53, 0x42800000, v53
	v_med3_f32 v60, v52, s50, v51
	v_med3_f32 v53, v53, s50, v51
	v_mov_b32_e32 v52, v3
	v_cvt_pk_fp8_f32 v52, v60, v53
	v_mul_f32_e32 v53, 0x42800000, v55
	v_med3_f32 v54, v54, s50, v51
	v_med3_f32 v53, v53, s50, v51
	v_cvt_pk_fp8_f32 v52, v54, v53 op_sel:[0,0,1]
	s_waitcnt lgkmcnt(1)
	v_mul_f32_e32 v53, 0x42800000, v56
	v_mul_f32_e32 v54, 0x42800000, v57
	v_med3_f32 v56, v53, s50, v51
	v_med3_f32 v54, v54, s50, v51
	v_mov_b32_e32 v53, v3
	v_cvt_pk_fp8_f32 v53, v56, v54
	s_waitcnt lgkmcnt(0)
	v_mul_f32_e32 v55, 0x42800000, v58
	v_mul_f32_e32 v54, 0x42800000, v59
	v_med3_f32 v55, v55, s50, v51
	v_med3_f32 v54, v54, s50, v51
	v_cvt_pk_fp8_f32 v53, v55, v54 op_sel:[0,0,1]
	v_or_b32_e32 v54, s8, v13
	v_lshlrev_b32_e32 v54, 11, v54
	v_mov_b32_e32 v55, v3
	ds_read2_b32 v[56:57], v26 offset1:1
	v_lshl_add_u64 v[54:55], v[10:11], 0, v[54:55]
	global_store_dwordx2 v[54:55], v[52:53], off nt
	ds_read2_b32 v[52:53], v26 offset0:2 offset1:3
	ds_read2_b32 v[54:55], v26 offset0:4 offset1:5
	ds_read2_b32 v[58:59], v26 offset0:6 offset1:7
	s_waitcnt lgkmcnt(3)
	v_mul_f32_e32 v56, 0x42800000, v56
	v_mul_f32_e32 v57, 0x42800000, v57
	s_waitcnt lgkmcnt(2)
	v_mul_f32_e32 v60, 0x42800000, v52
	v_med3_f32 v56, v56, s50, v51
	v_med3_f32 v57, v57, s50, v51
	v_mov_b32_e32 v52, v3
	v_cvt_pk_fp8_f32 v52, v56, v57
	v_mul_f32_e32 v53, 0x42800000, v53
	v_med3_f32 v56, v60, s50, v51
	v_med3_f32 v53, v53, s50, v51
	v_cvt_pk_fp8_f32 v52, v56, v53 op_sel:[0,0,1]
	s_waitcnt lgkmcnt(1)
	v_mul_f32_e32 v53, 0x42800000, v54
	v_mul_f32_e32 v54, 0x42800000, v55
	v_med3_f32 v56, v53, s50, v51
	v_med3_f32 v54, v54, s50, v51
	v_mov_b32_e32 v53, v3
	v_cvt_pk_fp8_f32 v53, v56, v54
	s_waitcnt lgkmcnt(0)
	v_mul_f32_e32 v55, 0x42800000, v58
	v_mul_f32_e32 v54, 0x42800000, v59
	v_med3_f32 v55, v55, s50, v51
	v_med3_f32 v54, v54, s50, v51
	v_cvt_pk_fp8_f32 v53, v55, v54 op_sel:[0,0,1]
	v_or_b32_e32 v54, s8, v15
	v_lshlrev_b32_e32 v54, 11, v54
	v_mov_b32_e32 v55, v3
	ds_read2_b32 v[56:57], v27 offset1:1
	v_lshl_add_u64 v[54:55], v[10:11], 0, v[54:55]
	global_store_dwordx2 v[54:55], v[52:53], off nt
	ds_read2_b32 v[52:53], v28 offset1:1
	ds_read2_b32 v[54:55], v29 offset1:1
	ds_read2_b32 v[58:59], v30 offset1:1
	s_waitcnt lgkmcnt(3)
	v_mul_f32_e32 v56, 0x42800000, v56
	v_mul_f32_e32 v57, 0x42800000, v57
	s_waitcnt lgkmcnt(2)
	v_mul_f32_e32 v60, 0x42800000, v52
	v_med3_f32 v56, v56, s50, v51
	v_med3_f32 v57, v57, s50, v51
	v_mov_b32_e32 v52, v3
	v_cvt_pk_fp8_f32 v52, v56, v57
	v_mul_f32_e32 v53, 0x42800000, v53
	v_med3_f32 v56, v60, s50, v51
	v_med3_f32 v53, v53, s50, v51
	v_cvt_pk_fp8_f32 v52, v56, v53 op_sel:[0,0,1]
	s_waitcnt lgkmcnt(1)
	v_mul_f32_e32 v53, 0x42800000, v54
	v_mul_f32_e32 v54, 0x42800000, v55
	v_med3_f32 v56, v53, s50, v51
	v_med3_f32 v54, v54, s50, v51
	v_mov_b32_e32 v53, v3
	v_cvt_pk_fp8_f32 v53, v56, v54
	s_waitcnt lgkmcnt(0)
	v_mul_f32_e32 v55, 0x42800000, v58
	v_mul_f32_e32 v54, 0x42800000, v59
	v_med3_f32 v55, v55, s50, v51
	v_med3_f32 v54, v54, s50, v51
	v_cvt_pk_fp8_f32 v53, v55, v54 op_sel:[0,0,1]
	v_or_b32_e32 v54, s8, v16
	v_lshlrev_b32_e32 v54, 11, v54
	v_mov_b32_e32 v55, v3
	ds_read2_b32 v[56:57], v31 offset1:1
	v_lshl_add_u64 v[54:55], v[10:11], 0, v[54:55]
	global_store_dwordx2 v[54:55], v[52:53], off nt
	ds_read2_b32 v[52:53], v32 offset1:1
	ds_read2_b32 v[54:55], v33 offset1:1
	ds_read2_b32 v[58:59], v34 offset1:1
	s_waitcnt lgkmcnt(3)
	v_mul_f32_e32 v56, 0x42800000, v56
	v_mul_f32_e32 v57, 0x42800000, v57
	s_waitcnt lgkmcnt(2)
	v_mul_f32_e32 v60, 0x42800000, v52
	v_med3_f32 v56, v56, s50, v51
	v_med3_f32 v57, v57, s50, v51
	v_mov_b32_e32 v52, v3
	v_cvt_pk_fp8_f32 v52, v56, v57
	v_mul_f32_e32 v53, 0x42800000, v53
	v_med3_f32 v56, v60, s50, v51
	v_med3_f32 v53, v53, s50, v51
	v_cvt_pk_fp8_f32 v52, v56, v53 op_sel:[0,0,1]
	s_waitcnt lgkmcnt(1)
	v_mul_f32_e32 v53, 0x42800000, v54
	v_mul_f32_e32 v54, 0x42800000, v55
	v_med3_f32 v56, v53, s50, v51
	v_med3_f32 v54, v54, s50, v51
	v_mov_b32_e32 v53, v3
	v_cvt_pk_fp8_f32 v53, v56, v54
	s_waitcnt lgkmcnt(0)
	v_mul_f32_e32 v55, 0x42800000, v58
	v_mul_f32_e32 v54, 0x42800000, v59
	v_med3_f32 v55, v55, s50, v51
	v_med3_f32 v54, v54, s50, v51
	v_cvt_pk_fp8_f32 v53, v55, v54 op_sel:[0,0,1]
	v_or_b32_e32 v54, s8, v17
	v_lshlrev_b32_e32 v54, 11, v54
	v_mov_b32_e32 v55, v3
	ds_read2_b32 v[56:57], v35 offset1:1
	v_lshl_add_u64 v[54:55], v[10:11], 0, v[54:55]
	global_store_dwordx2 v[54:55], v[52:53], off nt
	ds_read2_b32 v[52:53], v36 offset1:1
	ds_read2_b32 v[54:55], v37 offset1:1
	ds_read2_b32 v[58:59], v38 offset1:1
	s_waitcnt lgkmcnt(3)
	v_mul_f32_e32 v56, 0x42800000, v56
	v_mul_f32_e32 v57, 0x42800000, v57
	s_waitcnt lgkmcnt(2)
	v_mul_f32_e32 v60, 0x42800000, v52
	v_med3_f32 v56, v56, s50, v51
	v_med3_f32 v57, v57, s50, v51
	v_mov_b32_e32 v52, v3
	v_cvt_pk_fp8_f32 v52, v56, v57
	v_mul_f32_e32 v53, 0x42800000, v53
	v_med3_f32 v56, v60, s50, v51
	v_med3_f32 v53, v53, s50, v51
	v_cvt_pk_fp8_f32 v52, v56, v53 op_sel:[0,0,1]
	s_waitcnt lgkmcnt(1)
	v_mul_f32_e32 v53, 0x42800000, v54
	v_mul_f32_e32 v54, 0x42800000, v55
	v_med3_f32 v56, v53, s50, v51
	v_med3_f32 v54, v54, s50, v51
	v_mov_b32_e32 v53, v3
	v_cvt_pk_fp8_f32 v53, v56, v54
	s_waitcnt lgkmcnt(0)
	v_mul_f32_e32 v55, 0x42800000, v58
	v_mul_f32_e32 v54, 0x42800000, v59
	v_med3_f32 v55, v55, s50, v51
	v_med3_f32 v54, v54, s50, v51
	v_cvt_pk_fp8_f32 v53, v55, v54 op_sel:[0,0,1]
	v_or_b32_e32 v54, s8, v18
	v_lshlrev_b32_e32 v54, 11, v54
	v_mov_b32_e32 v55, v3
	ds_read2_b32 v[56:57], v39 offset1:1
	v_lshl_add_u64 v[54:55], v[10:11], 0, v[54:55]
	global_store_dwordx2 v[54:55], v[52:53], off nt
	ds_read2_b32 v[52:53], v40 offset1:1
	ds_read2_b32 v[54:55], v41 offset1:1
	ds_read2_b32 v[58:59], v42 offset1:1
	s_waitcnt lgkmcnt(3)
	v_mul_f32_e32 v56, 0x42800000, v56
	v_mul_f32_e32 v57, 0x42800000, v57
	s_waitcnt lgkmcnt(2)
	v_mul_f32_e32 v60, 0x42800000, v52
	v_med3_f32 v56, v56, s50, v51
	v_med3_f32 v57, v57, s50, v51
	v_mov_b32_e32 v52, v3
	v_cvt_pk_fp8_f32 v52, v56, v57
	v_mul_f32_e32 v53, 0x42800000, v53
	v_med3_f32 v56, v60, s50, v51
	v_med3_f32 v53, v53, s50, v51
	v_cvt_pk_fp8_f32 v52, v56, v53 op_sel:[0,0,1]
	s_waitcnt lgkmcnt(1)
	v_mul_f32_e32 v53, 0x42800000, v54
	v_mul_f32_e32 v54, 0x42800000, v55
	v_med3_f32 v56, v53, s50, v51
	v_med3_f32 v54, v54, s50, v51
	v_mov_b32_e32 v53, v3
	v_cvt_pk_fp8_f32 v53, v56, v54
	s_waitcnt lgkmcnt(0)
	v_mul_f32_e32 v55, 0x42800000, v58
	v_mul_f32_e32 v54, 0x42800000, v59
	v_med3_f32 v55, v55, s50, v51
	v_med3_f32 v54, v54, s50, v51
	v_cvt_pk_fp8_f32 v53, v55, v54 op_sel:[0,0,1]
	v_or_b32_e32 v54, s8, v19
	v_lshlrev_b32_e32 v54, 11, v54
	v_mov_b32_e32 v55, v3
	ds_read2_b32 v[56:57], v43 offset1:1
	v_lshl_add_u64 v[54:55], v[10:11], 0, v[54:55]
	global_store_dwordx2 v[54:55], v[52:53], off nt
	ds_read2_b32 v[52:53], v44 offset1:1
	ds_read2_b32 v[54:55], v45 offset1:1
	ds_read2_b32 v[58:59], v46 offset1:1
	s_waitcnt lgkmcnt(3)
	v_mul_f32_e32 v56, 0x42800000, v56
	v_mul_f32_e32 v57, 0x42800000, v57
	s_waitcnt lgkmcnt(2)
	v_mul_f32_e32 v60, 0x42800000, v52
	v_med3_f32 v56, v56, s50, v51
	v_med3_f32 v57, v57, s50, v51
	v_mov_b32_e32 v52, v3
	v_cvt_pk_fp8_f32 v52, v56, v57
	v_mul_f32_e32 v53, 0x42800000, v53
	v_med3_f32 v56, v60, s50, v51
	v_med3_f32 v53, v53, s50, v51
	v_cvt_pk_fp8_f32 v52, v56, v53 op_sel:[0,0,1]
	s_waitcnt lgkmcnt(1)
	v_mul_f32_e32 v53, 0x42800000, v54
	v_mul_f32_e32 v54, 0x42800000, v55
	v_med3_f32 v56, v53, s50, v51
	v_med3_f32 v54, v54, s50, v51
	v_mov_b32_e32 v53, v3
	v_cvt_pk_fp8_f32 v53, v56, v54
	s_waitcnt lgkmcnt(0)
	v_mul_f32_e32 v55, 0x42800000, v58
	v_mul_f32_e32 v54, 0x42800000, v59
	v_med3_f32 v55, v55, s50, v51
	v_med3_f32 v54, v54, s50, v51
	v_cvt_pk_fp8_f32 v53, v55, v54 op_sel:[0,0,1]
	v_or_b32_e32 v54, s8, v20
	v_lshlrev_b32_e32 v54, 11, v54
	v_mov_b32_e32 v55, v3
	ds_read2_b32 v[56:57], v47 offset1:1
	v_lshl_add_u64 v[54:55], v[10:11], 0, v[54:55]
	global_store_dwordx2 v[54:55], v[52:53], off nt
	ds_read2_b32 v[52:53], v48 offset1:1
	ds_read2_b32 v[54:55], v49 offset1:1
	ds_read2_b32 v[58:59], v50 offset1:1
	s_waitcnt lgkmcnt(3)
	v_mul_f32_e32 v56, 0x42800000, v56
	v_mul_f32_e32 v57, 0x42800000, v57
	s_waitcnt lgkmcnt(2)
	v_mul_f32_e32 v60, 0x42800000, v52
	v_med3_f32 v56, v56, s50, v51
	v_med3_f32 v57, v57, s50, v51
	v_mov_b32_e32 v52, v3
	v_cvt_pk_fp8_f32 v52, v56, v57
	v_mul_f32_e32 v53, 0x42800000, v53
	v_med3_f32 v56, v60, s50, v51
	v_med3_f32 v53, v53, s50, v51
	v_cvt_pk_fp8_f32 v52, v56, v53 op_sel:[0,0,1]
	s_waitcnt lgkmcnt(1)
	v_mul_f32_e32 v53, 0x42800000, v54
	v_mul_f32_e32 v54, 0x42800000, v55
	v_med3_f32 v56, v53, s50, v51
	v_med3_f32 v54, v54, s50, v51
	v_mov_b32_e32 v53, v3
	v_cvt_pk_fp8_f32 v53, v56, v54
	s_waitcnt lgkmcnt(0)
	v_mul_f32_e32 v55, 0x42800000, v58
	v_mul_f32_e32 v54, 0x42800000, v59
	v_med3_f32 v55, v55, s50, v51
	v_med3_f32 v54, v54, s50, v51
	v_cvt_pk_fp8_f32 v53, v55, v54 op_sel:[0,0,1]
	v_or_b32_e32 v54, s8, v21
	v_lshlrev_b32_e32 v54, 11, v54
	v_mov_b32_e32 v55, v3
	v_lshl_add_u64 v[10:11], v[10:11], 0, v[54:55]
	global_store_dwordx2 v[10:11], v[52:53], off nt
	s_waitcnt lgkmcnt(0)
.LBB0_47:
	s_andn2_b64 vcc, exec, s[14:15]
	s_cbranch_vccnz .LBB0_49
	s_add_i32 s8, s90, 0xfffff980
	s_bfe_u32 s40, s8, 0x40009
	s_bfe_u32 s42, s8, 0x50004
	s_cmpk_lt_u32 s8, 0x2000
	s_movk_i32 s14, 0xb8
	s_cselect_b32 s14, s14, 0xc0
	s_add_u32 s14, s28, s14
	s_addc_u32 s15, s29, 0
	s_load_dwordx2 s[14:15], s[14:15], 0x0
	s_lshl_b64 s[44:45], s[12:13], 4
	s_or_b32 s44, s44, s40
	s_lshl_b64 s[92:93], s[44:45], 23
	v_mov_b32_e32 v53, v3
	s_waitcnt lgkmcnt(0)
	s_add_u32 s40, s14, s92
	s_addc_u32 s91, s15, s93
	s_lshl_b64 s[14:15], s[44:45], 22
	s_add_u32 s44, s16, s14
	s_addc_u32 s45, s17, s15
	s_lshr_b32 s8, s8, 10
	s_lshl_b32 s14, s42, 7
	s_and_b32 s8, s8, 0x3ffff8
	s_and_b32 s92, s85, 0x3c0
	s_add_i32 s8, s14, s8
	s_lshl_b32 s14, s42, 8
	s_add_u32 s14, s40, s14
	v_or_b32_e32 v52, s92, v9
	s_addc_u32 s15, s91, 0
	v_lshl_add_u64 v[10:11], s[14:15], 0, v[2:3]
	v_lshlrev_b32_e32 v52, 13, v52
	v_lshl_add_u64 v[10:11], v[10:11], 0, v[52:53]
	v_add_co_u32_e32 v56, vcc, s31, v10
	s_mov_b32 s14, 0x40000
	s_nop 0
	v_addc_co_u32_e32 v57, vcc, 0, v11, vcc
	v_add_co_u32_e32 v60, vcc, s34, v10
	global_load_dwordx4 v[52:55], v[10:11], off nt
	s_nop 0
	global_load_dwordx4 v[56:59], v[56:57], off nt
	v_addc_co_u32_e32 v61, vcc, 0, v11, vcc
	v_add_co_u32_e32 v64, vcc, s36, v10
	s_nop 1
	v_addc_co_u32_e32 v65, vcc, 0, v11, vcc
	v_add_co_u32_e32 v68, vcc, s38, v10
	global_load_dwordx4 v[60:63], v[60:61], off nt
	s_nop 0
	global_load_dwordx4 v[64:67], v[64:65], off nt
	v_addc_co_u32_e32 v69, vcc, 0, v11, vcc
	v_add_co_u32_e32 v72, vcc, s41, v10
	s_nop 1
	v_addc_co_u32_e32 v73, vcc, 0, v11, vcc
	v_add_co_u32_e32 v76, vcc, s46, v10
	global_load_dwordx4 v[68:71], v[68:69], off nt
	s_nop 0
	global_load_dwordx4 v[72:75], v[72:73], off nt
	v_addc_co_u32_e32 v77, vcc, 0, v11, vcc
	v_add_co_u32_e32 v80, vcc, s48, v10
	s_nop 1
	v_addc_co_u32_e32 v81, vcc, 0, v11, vcc
	v_add_co_u32_e32 v84, vcc, s14, v10
	s_mov_b32 s14, 0x48000
	s_nop 0
	v_addc_co_u32_e32 v85, vcc, 0, v11, vcc
	v_add_co_u32_e32 v88, vcc, s14, v10
	s_mov_b32 s14, 0x50000
	s_nop 0
	v_addc_co_u32_e32 v89, vcc, 0, v11, vcc
	v_add_co_u32_e32 v92, vcc, s14, v10
	s_mov_b32 s14, 0x58000
	s_nop 0
	v_addc_co_u32_e32 v93, vcc, 0, v11, vcc
	v_add_co_u32_e32 v96, vcc, s14, v10
	s_mov_b32 s14, 0x68000
	s_nop 0
	v_addc_co_u32_e32 v97, vcc, 0, v11, vcc
	v_add_co_u32_e32 v100, vcc, s51, v10
	global_load_dwordx4 v[76:79], v[76:77], off nt
	s_nop 0
	global_load_dwordx4 v[80:83], v[80:81], off nt
	v_addc_co_u32_e32 v101, vcc, 0, v11, vcc
	v_add_co_u32_e32 v104, vcc, s14, v10
	s_mov_b32 s14, 0x70000
	s_nop 0
	v_addc_co_u32_e32 v105, vcc, 0, v11, vcc
	v_add_co_u32_e32 v108, vcc, s14, v10
	s_mov_b32 s14, 0x78000
	s_nop 0
	v_addc_co_u32_e32 v109, vcc, 0, v11, vcc
	v_add_co_u32_e32 v10, vcc, s14, v10
	global_load_dwordx4 v[84:87], v[84:85], off nt
	s_nop 0
	global_load_dwordx4 v[88:91], v[88:89], off nt
	s_nop 0
	global_load_dwordx4 v[92:95], v[92:93], off nt
	s_nop 0
	global_load_dwordx4 v[96:99], v[96:97], off nt
	s_nop 0
	global_load_dwordx4 v[100:103], v[100:101], off nt
	s_nop 0
	global_load_dwordx4 v[104:107], v[104:105], off nt
	v_addc_co_u32_e32 v11, vcc, 0, v11, vcc
	global_load_dwordx4 v[108:111], v[108:109], off nt
	s_nop 0
	global_load_dwordx4 v[112:115], v[10:11], off nt
	s_add_u32 s14, s44, s92
	s_addc_u32 s15, s45, 0
	v_lshl_add_u64 v[10:11], s[14:15], 0, v[4:5]
	s_waitcnt vmcnt(14)
	ds_write2_b32 v12, v52, v56 offset1:4
	ds_write2_b32 v12, v53, v57 offset0:65 offset1:69
	ds_write2_b32 v12, v54, v58 offset0:130 offset1:134
	ds_write2_b32 v12, v55, v59 offset0:195 offset1:199
	s_waitcnt vmcnt(12)
	ds_write2_b32 v12, v60, v64 offset0:8 offset1:12
	ds_write2_b32 v12, v61, v65 offset0:73 offset1:77
	ds_write2_b32 v12, v62, v66 offset0:138 offset1:142
	ds_write2_b32 v12, v63, v67 offset0:203 offset1:207
	s_waitcnt vmcnt(10)
	ds_write2_b32 v12, v68, v72 offset0:16 offset1:20
	ds_write2_b32 v12, v69, v73 offset0:81 offset1:85
	ds_write2_b32 v12, v70, v74 offset0:146 offset1:150
	ds_write2_b32 v12, v71, v75 offset0:211 offset1:215
	s_waitcnt vmcnt(8)
	ds_write2_b32 v12, v76, v80 offset0:24 offset1:28
	ds_write2_b32 v12, v77, v81 offset0:89 offset1:93
	ds_write2_b32 v12, v78, v82 offset0:154 offset1:158
	ds_write2_b32 v12, v79, v83 offset0:219 offset1:223
	s_waitcnt vmcnt(6)
	ds_write2_b32 v12, v84, v88 offset0:32 offset1:36
	ds_write2_b32 v12, v85, v89 offset0:97 offset1:101
	ds_write2_b32 v12, v86, v90 offset0:162 offset1:166
	ds_write2_b32 v12, v87, v91 offset0:227 offset1:231
	s_waitcnt vmcnt(4)
	ds_write2_b32 v12, v92, v96 offset0:40 offset1:44
	ds_write2_b32 v12, v93, v97 offset0:105 offset1:109
	ds_write2_b32 v12, v94, v98 offset0:170 offset1:174
	ds_write2_b32 v12, v95, v99 offset0:235 offset1:239
	s_waitcnt vmcnt(2)
	ds_write2_b32 v12, v100, v104 offset0:48 offset1:52
	ds_write2_b32 v12, v101, v105 offset0:113 offset1:117
	ds_write2_b32 v12, v102, v106 offset0:178 offset1:182
	ds_write2_b32 v12, v103, v107 offset0:243 offset1:247
	s_waitcnt vmcnt(0)
	ds_write2_b32 v12, v108, v112 offset0:56 offset1:60
	ds_write2_b32 v12, v109, v113 offset0:121 offset1:125
	ds_write2_b32 v12, v110, v114 offset0:186 offset1:190
	ds_write2_b32 v12, v111, v115 offset0:251 offset1:255
	s_waitcnt lgkmcnt(0)
	ds_read2_b32 v[52:53], v14 offset1:1
	ds_read2_b32 v[54:55], v14 offset0:2 offset1:3
	ds_read2_b32 v[56:57], v14 offset0:4 offset1:5
	ds_read2_b32 v[58:59], v14 offset0:6 offset1:7
	s_waitcnt lgkmcnt(2)
	v_mul_f32_e32 v54, 0x42800000, v54
	v_mul_f32_e32 v52, 0x42800000, v52
	v_mul_f32_e32 v53, 0x42800000, v53
	v_med3_f32 v60, v52, s50, v51
	v_med3_f32 v53, v53, s50, v51
	v_mov_b32_e32 v52, v3
	v_cvt_pk_fp8_f32 v52, v60, v53
	v_mul_f32_e32 v53, 0x42800000, v55
	v_med3_f32 v54, v54, s50, v51
	v_med3_f32 v53, v53, s50, v51
	v_cvt_pk_fp8_f32 v52, v54, v53 op_sel:[0,0,1]
	s_waitcnt lgkmcnt(1)
	v_mul_f32_e32 v53, 0x42800000, v56
	v_mul_f32_e32 v54, 0x42800000, v57
	v_med3_f32 v56, v53, s50, v51
	v_med3_f32 v54, v54, s50, v51
	v_mov_b32_e32 v53, v3
	v_cvt_pk_fp8_f32 v53, v56, v54
	s_waitcnt lgkmcnt(0)
	v_mul_f32_e32 v55, 0x42800000, v58
	v_mul_f32_e32 v54, 0x42800000, v59
	v_med3_f32 v55, v55, s50, v51
	v_med3_f32 v54, v54, s50, v51
	v_cvt_pk_fp8_f32 v53, v55, v54 op_sel:[0,0,1]
	v_or_b32_e32 v54, s8, v13
	v_mov_b32_e32 v55, v3
	v_lshlrev_b64 v[54:55], 10, v[54:55]
	v_lshl_add_u64 v[54:55], v[10:11], 0, v[54:55]
	global_store_dwordx2 v[54:55], v[52:53], off nt
	v_add_u32_e32 v52, 0x820, v14
	ds_read2_b32 v[52:53], v52 offset1:1
	v_add_u32_e32 v54, 0x828, v14
	v_add_u32_e32 v56, 0x830, v14
	v_add_u32_e32 v58, 0x838, v14
	ds_read2_b32 v[54:55], v54 offset1:1
	ds_read2_b32 v[56:57], v56 offset1:1
	ds_read2_b32 v[58:59], v58 offset1:1
	s_waitcnt lgkmcnt(3)
	v_mul_f32_e32 v52, 0x42800000, v52
	v_mul_f32_e32 v53, 0x42800000, v53
	v_med3_f32 v60, v52, s50, v51
	v_med3_f32 v53, v53, s50, v51
	v_mov_b32_e32 v52, v3
	v_cvt_pk_fp8_f32 v52, v60, v53
	s_waitcnt lgkmcnt(2)
	v_mul_f32_e32 v54, 0x42800000, v54
	v_mul_f32_e32 v53, 0x42800000, v55
	v_med3_f32 v54, v54, s50, v51
	v_med3_f32 v53, v53, s50, v51
	v_cvt_pk_fp8_f32 v52, v54, v53 op_sel:[0,0,1]
	s_waitcnt lgkmcnt(1)
	v_mul_f32_e32 v53, 0x42800000, v56
	v_mul_f32_e32 v54, 0x42800000, v57
	v_med3_f32 v56, v53, s50, v51
	v_med3_f32 v54, v54, s50, v51
	v_mov_b32_e32 v53, v3
	v_cvt_pk_fp8_f32 v53, v56, v54
	s_waitcnt lgkmcnt(0)
	v_mul_f32_e32 v55, 0x42800000, v58
	v_mul_f32_e32 v54, 0x42800000, v59
	v_med3_f32 v55, v55, s50, v51
	v_med3_f32 v54, v54, s50, v51
	v_cvt_pk_fp8_f32 v53, v55, v54 op_sel:[0,0,1]
	v_add_u32_e32 v54, s8, v16
	v_mov_b32_e32 v55, v3
	v_lshlrev_b64 v[54:55], 10, v[54:55]
	ds_read2_b32 v[56:57], v27 offset1:1
	v_lshl_add_u64 v[54:55], v[10:11], 0, v[54:55]
	global_store_dwordx2 v[54:55], v[52:53], off nt
	ds_read2_b32 v[52:53], v28 offset1:1
	ds_read2_b32 v[54:55], v29 offset1:1
	ds_read2_b32 v[58:59], v30 offset1:1
	s_waitcnt lgkmcnt(3)
	v_mul_f32_e32 v56, 0x42800000, v56
	v_mul_f32_e32 v57, 0x42800000, v57
	s_waitcnt lgkmcnt(2)
	v_mul_f32_e32 v60, 0x42800000, v52
	v_med3_f32 v56, v56, s50, v51
	v_med3_f32 v57, v57, s50, v51
	v_mov_b32_e32 v52, v3
	v_cvt_pk_fp8_f32 v52, v56, v57
	v_mul_f32_e32 v53, 0x42800000, v53
	v_med3_f32 v56, v60, s50, v51
	v_med3_f32 v53, v53, s50, v51
	v_cvt_pk_fp8_f32 v52, v56, v53 op_sel:[0,0,1]
	s_waitcnt lgkmcnt(1)
	v_mul_f32_e32 v53, 0x42800000, v54
	v_mul_f32_e32 v54, 0x42800000, v55
	v_med3_f32 v56, v53, s50, v51
	v_med3_f32 v54, v54, s50, v51
	v_mov_b32_e32 v53, v3
	v_cvt_pk_fp8_f32 v53, v56, v54
	s_waitcnt lgkmcnt(0)
	v_mul_f32_e32 v55, 0x42800000, v58
	v_mul_f32_e32 v54, 0x42800000, v59
	v_med3_f32 v55, v55, s50, v51
	v_med3_f32 v54, v54, s50, v51
	v_cvt_pk_fp8_f32 v53, v55, v54 op_sel:[0,0,1]
	v_add_u32_e32 v54, s8, v18
	v_mov_b32_e32 v55, v3
	v_lshlrev_b64 v[54:55], 10, v[54:55]
	v_lshl_add_u64 v[54:55], v[10:11], 0, v[54:55]
	global_store_dwordx2 v[54:55], v[52:53], off nt
	v_add_u32_e32 v52, 0x1860, v14
	ds_read2_b32 v[52:53], v52 offset1:1
	v_add_u32_e32 v54, 0x1868, v14
	v_add_u32_e32 v56, 0x1870, v14
	v_add_u32_e32 v58, 0x1878, v14
	ds_read2_b32 v[54:55], v54 offset1:1
	ds_read2_b32 v[56:57], v56 offset1:1
	ds_read2_b32 v[58:59], v58 offset1:1
	s_waitcnt lgkmcnt(3)
	v_mul_f32_e32 v52, 0x42800000, v52
	v_mul_f32_e32 v53, 0x42800000, v53
	v_med3_f32 v60, v52, s50, v51
	v_med3_f32 v53, v53, s50, v51
	v_mov_b32_e32 v52, v3
	v_cvt_pk_fp8_f32 v52, v60, v53
	s_waitcnt lgkmcnt(2)
	v_mul_f32_e32 v54, 0x42800000, v54
	v_mul_f32_e32 v53, 0x42800000, v55
	v_med3_f32 v54, v54, s50, v51
	v_med3_f32 v53, v53, s50, v51
	v_cvt_pk_fp8_f32 v52, v54, v53 op_sel:[0,0,1]
	s_waitcnt lgkmcnt(1)
	v_mul_f32_e32 v53, 0x42800000, v56
	v_mul_f32_e32 v54, 0x42800000, v57
	v_med3_f32 v56, v53, s50, v51
	v_med3_f32 v54, v54, s50, v51
	v_mov_b32_e32 v53, v3
	v_cvt_pk_fp8_f32 v53, v56, v54
	s_waitcnt lgkmcnt(0)
	v_mul_f32_e32 v55, 0x42800000, v58
	v_mul_f32_e32 v54, 0x42800000, v59
	v_med3_f32 v55, v55, s50, v51
	v_med3_f32 v54, v54, s50, v51
	v_cvt_pk_fp8_f32 v53, v55, v54 op_sel:[0,0,1]
	v_add_u32_e32 v54, s8, v20
	v_mov_b32_e32 v55, v3
	v_lshlrev_b64 v[54:55], 10, v[54:55]
	ds_read2_b32 v[56:57], v35 offset1:1
	v_lshl_add_u64 v[54:55], v[10:11], 0, v[54:55]
	global_store_dwordx2 v[54:55], v[52:53], off nt
	ds_read2_b32 v[52:53], v36 offset1:1
	ds_read2_b32 v[54:55], v37 offset1:1
	ds_read2_b32 v[58:59], v38 offset1:1
	s_waitcnt lgkmcnt(3)
	v_mul_f32_e32 v56, 0x42800000, v56
	v_mul_f32_e32 v57, 0x42800000, v57
	s_waitcnt lgkmcnt(2)
	v_mul_f32_e32 v60, 0x42800000, v52
	v_med3_f32 v56, v56, s50, v51
	v_med3_f32 v57, v57, s50, v51
	v_mov_b32_e32 v52, v3
	v_cvt_pk_fp8_f32 v52, v56, v57
	v_mul_f32_e32 v53, 0x42800000, v53
	v_med3_f32 v56, v60, s50, v51
	v_med3_f32 v53, v53, s50, v51
	v_cvt_pk_fp8_f32 v52, v56, v53 op_sel:[0,0,1]
	s_waitcnt lgkmcnt(1)
	v_mul_f32_e32 v53, 0x42800000, v54
	v_mul_f32_e32 v54, 0x42800000, v55
	v_med3_f32 v56, v53, s50, v51
	v_med3_f32 v54, v54, s50, v51
	v_mov_b32_e32 v53, v3
	v_cvt_pk_fp8_f32 v53, v56, v54
	s_waitcnt lgkmcnt(0)
	v_mul_f32_e32 v55, 0x42800000, v58
	v_mul_f32_e32 v54, 0x42800000, v59
	v_med3_f32 v55, v55, s50, v51
	v_med3_f32 v54, v54, s50, v51
	v_cvt_pk_fp8_f32 v53, v55, v54 op_sel:[0,0,1]
	v_add_u32_e32 v54, s8, v22
	v_mov_b32_e32 v55, v3
	v_lshlrev_b64 v[54:55], 10, v[54:55]
	v_lshl_add_u64 v[54:55], v[10:11], 0, v[54:55]
	global_store_dwordx2 v[54:55], v[52:53], off nt
	v_add_u32_e32 v52, 0x28a0, v14
	ds_read2_b32 v[52:53], v52 offset1:1
	v_add_u32_e32 v54, 0x28a8, v14
	v_add_u32_e32 v56, 0x28b0, v14
	v_add_u32_e32 v58, 0x28b8, v14
	ds_read2_b32 v[54:55], v54 offset1:1
	ds_read2_b32 v[56:57], v56 offset1:1
	ds_read2_b32 v[58:59], v58 offset1:1
	s_waitcnt lgkmcnt(3)
	v_mul_f32_e32 v52, 0x42800000, v52
	v_mul_f32_e32 v53, 0x42800000, v53
	v_med3_f32 v60, v52, s50, v51
	v_med3_f32 v53, v53, s50, v51
	v_mov_b32_e32 v52, v3
	v_cvt_pk_fp8_f32 v52, v60, v53
	s_waitcnt lgkmcnt(2)
	v_mul_f32_e32 v54, 0x42800000, v54
	v_mul_f32_e32 v53, 0x42800000, v55
	v_med3_f32 v54, v54, s50, v51
	v_med3_f32 v53, v53, s50, v51
	v_cvt_pk_fp8_f32 v52, v54, v53 op_sel:[0,0,1]
	s_waitcnt lgkmcnt(1)
	v_mul_f32_e32 v53, 0x42800000, v56
	v_mul_f32_e32 v54, 0x42800000, v57
	v_med3_f32 v56, v53, s50, v51
	v_med3_f32 v54, v54, s50, v51
	v_mov_b32_e32 v53, v3
	v_cvt_pk_fp8_f32 v53, v56, v54
	s_waitcnt lgkmcnt(0)
	v_mul_f32_e32 v55, 0x42800000, v58
	v_mul_f32_e32 v54, 0x42800000, v59
	v_med3_f32 v55, v55, s50, v51
	v_med3_f32 v54, v54, s50, v51
	v_cvt_pk_fp8_f32 v53, v55, v54 op_sel:[0,0,1]
	v_add_u32_e32 v54, s8, v23
	v_mov_b32_e32 v55, v3
	v_lshlrev_b64 v[54:55], 10, v[54:55]
	ds_read2_b32 v[56:57], v43 offset1:1
	v_lshl_add_u64 v[54:55], v[10:11], 0, v[54:55]
	global_store_dwordx2 v[54:55], v[52:53], off nt
	ds_read2_b32 v[52:53], v44 offset1:1
	ds_read2_b32 v[54:55], v45 offset1:1
	ds_read2_b32 v[58:59], v46 offset1:1
	s_waitcnt lgkmcnt(3)
	v_mul_f32_e32 v56, 0x42800000, v56
	v_mul_f32_e32 v57, 0x42800000, v57
	s_waitcnt lgkmcnt(2)
	v_mul_f32_e32 v60, 0x42800000, v52
	v_med3_f32 v56, v56, s50, v51
	v_med3_f32 v57, v57, s50, v51
	v_mov_b32_e32 v52, v3
	v_cvt_pk_fp8_f32 v52, v56, v57
	v_mul_f32_e32 v53, 0x42800000, v53
	v_med3_f32 v56, v60, s50, v51
	v_med3_f32 v53, v53, s50, v51
	v_cvt_pk_fp8_f32 v52, v56, v53 op_sel:[0,0,1]
	s_waitcnt lgkmcnt(1)
	v_mul_f32_e32 v53, 0x42800000, v54
	v_mul_f32_e32 v54, 0x42800000, v55
	v_med3_f32 v56, v53, s50, v51
	v_med3_f32 v54, v54, s50, v51
	v_mov_b32_e32 v53, v3
	v_cvt_pk_fp8_f32 v53, v56, v54
	s_waitcnt lgkmcnt(0)
	v_mul_f32_e32 v55, 0x42800000, v58
	v_mul_f32_e32 v54, 0x42800000, v59
	v_med3_f32 v55, v55, s50, v51
	v_med3_f32 v54, v54, s50, v51
	v_cvt_pk_fp8_f32 v53, v55, v54 op_sel:[0,0,1]
	v_add_u32_e32 v54, s8, v24
	v_mov_b32_e32 v55, v3
	v_lshlrev_b64 v[54:55], 10, v[54:55]
	v_lshl_add_u64 v[54:55], v[10:11], 0, v[54:55]
	global_store_dwordx2 v[54:55], v[52:53], off nt
	v_add_u32_e32 v52, 0x38e0, v14
	ds_read2_b32 v[52:53], v52 offset1:1
	v_add_u32_e32 v54, 0x38e8, v14
	v_add_u32_e32 v56, 0x38f0, v14
	v_add_u32_e32 v58, 0x38f8, v14
	ds_read2_b32 v[54:55], v54 offset1:1
	ds_read2_b32 v[56:57], v56 offset1:1
	ds_read2_b32 v[58:59], v58 offset1:1
	s_waitcnt lgkmcnt(3)
	v_mul_f32_e32 v52, 0x42800000, v52
	v_mul_f32_e32 v53, 0x42800000, v53
	v_med3_f32 v60, v52, s50, v51
	v_med3_f32 v53, v53, s50, v51
	v_mov_b32_e32 v52, v3
	v_cvt_pk_fp8_f32 v52, v60, v53
	s_waitcnt lgkmcnt(2)
	v_mul_f32_e32 v54, 0x42800000, v54
	v_mul_f32_e32 v53, 0x42800000, v55
	v_med3_f32 v54, v54, s50, v51
	v_med3_f32 v53, v53, s50, v51
	v_cvt_pk_fp8_f32 v52, v54, v53 op_sel:[0,0,1]
	s_waitcnt lgkmcnt(1)
	v_mul_f32_e32 v53, 0x42800000, v56
	v_mul_f32_e32 v54, 0x42800000, v57
	v_med3_f32 v56, v53, s50, v51
	v_med3_f32 v54, v54, s50, v51
	v_mov_b32_e32 v53, v3
	v_cvt_pk_fp8_f32 v53, v56, v54
	s_waitcnt lgkmcnt(0)
	v_mul_f32_e32 v55, 0x42800000, v58
	v_mul_f32_e32 v54, 0x42800000, v59
	v_med3_f32 v55, v55, s50, v51
	v_med3_f32 v54, v54, s50, v51
	v_cvt_pk_fp8_f32 v53, v55, v54 op_sel:[0,0,1]
	v_add_u32_e32 v54, s8, v25
	v_mov_b32_e32 v55, v3
	v_lshlrev_b64 v[54:55], 10, v[54:55]
	v_lshl_add_u64 v[10:11], v[10:11], 0, v[54:55]
	global_store_dwordx2 v[10:11], v[52:53], off nt
	s_waitcnt lgkmcnt(0)

.LBB0_50:
	s_andn2_b64 vcc, exec, s[14:15]
	s_cbranch_vccnz .LBB0_52
	s_load_dwordx2 s[14:15], s[28:29], 0xa8
	s_lshl_b64 s[44:45], s[12:13], 22
	s_mul_i32 s8, s12, 0xfffe6600
	v_mov_b32_e32 v53, v3
	s_waitcnt lgkmcnt(0)
	s_add_u32 s40, s14, s44
	s_addc_u32 s42, s15, s45
	s_add_i32 s8, s84, s8
	s_and_b32 s8, s8, 0x1fc0
	s_and_b32 s44, s85, 0x3c0
	s_addk_i32 s8, 0xea00
	s_lshl_b64 s[14:15], s[12:13], 21
	s_add_u32 s45, s18, s14
	s_addc_u32 s91, s19, s15
	s_lshl_b64 s[14:15], s[8:9], 2
	s_add_u32 s14, s40, s14
	v_or_b32_e32 v52, s44, v9
	s_addc_u32 s15, s42, s15
	v_lshl_add_u64 v[10:11], s[14:15], 0, v[2:3]
	v_lshlrev_b32_e32 v52, 12, v52
	v_lshl_add_u64 v[10:11], v[10:11], 0, v[52:53]
	v_add_co_u32_e32 v56, vcc, s30, v10
	s_lshl_b32 s14, s44, 1
	s_nop 0
	v_addc_co_u32_e32 v57, vcc, 0, v11, vcc
	v_add_co_u32_e32 v60, vcc, s31, v10
	global_load_dwordx4 v[52:55], v[10:11], off nt
	s_nop 0
	global_load_dwordx4 v[56:59], v[56:57], off nt
	v_addc_co_u32_e32 v61, vcc, 0, v11, vcc
	v_add_co_u32_e32 v64, vcc, s33, v10
	s_add_u32 s14, s45, s14
	s_nop 0
	v_addc_co_u32_e32 v65, vcc, 0, v11, vcc
	v_add_co_u32_e32 v68, vcc, s34, v10
	global_load_dwordx4 v[60:63], v[60:61], off nt
	s_nop 0
	global_load_dwordx4 v[64:67], v[64:65], off nt
	v_addc_co_u32_e32 v69, vcc, 0, v11, vcc
	v_add_co_u32_e32 v72, vcc, s35, v10
	s_addc_u32 s15, s91, 0
	s_nop 0
	v_addc_co_u32_e32 v73, vcc, 0, v11, vcc
	v_add_co_u32_e32 v76, vcc, s36, v10
	global_load_dwordx4 v[68:71], v[68:69], off nt
	s_nop 0
	global_load_dwordx4 v[72:75], v[72:73], off nt
	v_addc_co_u32_e32 v77, vcc, 0, v11, vcc
	v_add_co_u32_e32 v80, vcc, s37, v10
	s_nop 1
	v_addc_co_u32_e32 v81, vcc, 0, v11, vcc
	v_add_co_u32_e32 v84, vcc, s38, v10
	global_load_dwordx4 v[76:79], v[76:77], off nt
	s_nop 0
	global_load_dwordx4 v[80:83], v[80:81], off nt
	v_addc_co_u32_e32 v85, vcc, 0, v11, vcc
	v_add_co_u32_e32 v88, vcc, s39, v10
	s_nop 1
	v_addc_co_u32_e32 v89, vcc, 0, v11, vcc
	v_add_co_u32_e32 v92, vcc, s41, v10
	global_load_dwordx4 v[84:87], v[84:85], off nt
	s_nop 0
	global_load_dwordx4 v[88:91], v[88:89], off nt
	v_addc_co_u32_e32 v93, vcc, 0, v11, vcc
	v_add_co_u32_e32 v96, vcc, s43, v10
	s_nop 1
	v_addc_co_u32_e32 v97, vcc, 0, v11, vcc
	v_add_co_u32_e32 v100, vcc, s46, v10
	global_load_dwordx4 v[92:95], v[92:93], off nt
	s_nop 0
	global_load_dwordx4 v[96:99], v[96:97], off nt
	v_addc_co_u32_e32 v101, vcc, 0, v11, vcc
	v_add_co_u32_e32 v104, vcc, s47, v10
	s_nop 1
	v_addc_co_u32_e32 v105, vcc, 0, v11, vcc
	v_add_co_u32_e32 v108, vcc, s48, v10
	global_load_dwordx4 v[100:103], v[100:101], off nt
	s_nop 0
	global_load_dwordx4 v[104:107], v[104:105], off nt
	v_addc_co_u32_e32 v109, vcc, 0, v11, vcc
	v_add_co_u32_e32 v10, vcc, s49, v10
	s_nop 1
	v_addc_co_u32_e32 v11, vcc, 0, v11, vcc
	global_load_dwordx4 v[108:111], v[108:109], off nt
	s_nop 0
	global_load_dwordx4 v[112:115], v[10:11], off nt
	v_lshlrev_b32_e32 v10, 1, v4
	v_mov_b32_e32 v11, v3
	v_lshl_add_u64 v[10:11], s[14:15], 0, v[10:11]
	s_waitcnt vmcnt(14)
	ds_write2_b32 v12, v52, v56 offset1:4
	ds_write2_b32 v12, v53, v57 offset0:65 offset1:69
	ds_write2_b32 v12, v54, v58 offset0:130 offset1:134
	ds_write2_b32 v12, v55, v59 offset0:195 offset1:199
	s_waitcnt vmcnt(12)
	ds_write2_b32 v12, v60, v64 offset0:8 offset1:12
	ds_write2_b32 v12, v61, v65 offset0:73 offset1:77
	ds_write2_b32 v12, v62, v66 offset0:138 offset1:142
	ds_write2_b32 v12, v63, v67 offset0:203 offset1:207
	s_waitcnt vmcnt(10)
	ds_write2_b32 v12, v68, v72 offset0:16 offset1:20
	ds_write2_b32 v12, v69, v73 offset0:81 offset1:85
	ds_write2_b32 v12, v70, v74 offset0:146 offset1:150
	ds_write2_b32 v12, v71, v75 offset0:211 offset1:215
	s_waitcnt vmcnt(8)
	ds_write2_b32 v12, v76, v80 offset0:24 offset1:28
	ds_write2_b32 v12, v77, v81 offset0:89 offset1:93
	ds_write2_b32 v12, v78, v82 offset0:154 offset1:158
	ds_write2_b32 v12, v79, v83 offset0:219 offset1:223
	s_waitcnt vmcnt(6)
	ds_write2_b32 v12, v84, v88 offset0:32 offset1:36
	ds_write2_b32 v12, v85, v89 offset0:97 offset1:101
	ds_write2_b32 v12, v86, v90 offset0:162 offset1:166
	ds_write2_b32 v12, v87, v91 offset0:227 offset1:231
	s_waitcnt vmcnt(4)
	ds_write2_b32 v12, v92, v96 offset0:40 offset1:44
	ds_write2_b32 v12, v93, v97 offset0:105 offset1:109
	ds_write2_b32 v12, v94, v98 offset0:170 offset1:174
	ds_write2_b32 v12, v95, v99 offset0:235 offset1:239
	s_waitcnt vmcnt(2)
	ds_write2_b32 v12, v100, v104 offset0:48 offset1:52
	ds_write2_b32 v12, v101, v105 offset0:113 offset1:117
	ds_write2_b32 v12, v102, v106 offset0:178 offset1:182
	ds_write2_b32 v12, v103, v107 offset0:243 offset1:247
	s_waitcnt vmcnt(0)
	ds_write2_b32 v12, v108, v112 offset0:56 offset1:60
	ds_write2_b32 v12, v109, v113 offset0:121 offset1:125
	ds_write2_b32 v12, v110, v114 offset0:186 offset1:190
	ds_write2_b32 v12, v111, v115 offset0:251 offset1:255
	s_waitcnt lgkmcnt(0)
	ds_read2_b32 v[52:53], v14 offset1:1
	ds_read2_b32 v[54:55], v14 offset0:2 offset1:3
	ds_read2_b32 v[56:57], v14 offset0:4 offset1:5
	ds_read2_b32 v[58:59], v14 offset0:6 offset1:7
	s_waitcnt lgkmcnt(3)
	v_cvt_pk_bf16_f32 v52, v52, v53
	s_waitcnt lgkmcnt(2)
	v_cvt_pk_bf16_f32 v53, v54, v55
	s_waitcnt lgkmcnt(1)
	v_cvt_pk_bf16_f32 v54, v56, v57
	s_waitcnt lgkmcnt(0)
	v_cvt_pk_bf16_f32 v55, v58, v59
	ds_read2_b32 v[58:59], v26 offset1:1
	ds_read2_b32 v[60:61], v26 offset0:2 offset1:3
	ds_read2_b32 v[62:63], v26 offset0:4 offset1:5
	ds_read2_b32 v[64:65], v26 offset0:6 offset1:7
	v_or_b32_e32 v56, s8, v13
	v_mov_b32_e32 v57, v3
	v_lshlrev_b64 v[56:57], 11, v[56:57]
	v_lshl_add_u64 v[56:57], v[10:11], 0, v[56:57]
	global_store_dwordx4 v[56:57], v[52:55], off nt
	v_or_b32_e32 v56, s8, v15
	v_mov_b32_e32 v57, v3
	s_waitcnt lgkmcnt(3)
	v_cvt_pk_bf16_f32 v52, v58, v59
	s_waitcnt lgkmcnt(2)
	v_cvt_pk_bf16_f32 v53, v60, v61
	s_waitcnt lgkmcnt(1)
	v_cvt_pk_bf16_f32 v54, v62, v63
	s_waitcnt lgkmcnt(0)
	v_cvt_pk_bf16_f32 v55, v64, v65
	ds_read2_b32 v[58:59], v27 offset1:1
	ds_read2_b32 v[60:61], v28 offset1:1
	ds_read2_b32 v[62:63], v29 offset1:1
	ds_read2_b32 v[64:65], v30 offset1:1
	v_lshlrev_b64 v[56:57], 11, v[56:57]
	v_lshl_add_u64 v[56:57], v[10:11], 0, v[56:57]
	global_store_dwordx4 v[56:57], v[52:55], off nt
	v_or_b32_e32 v56, s8, v16
	v_mov_b32_e32 v57, v3
	s_waitcnt lgkmcnt(3)
	v_cvt_pk_bf16_f32 v52, v58, v59
	s_waitcnt lgkmcnt(2)
	v_cvt_pk_bf16_f32 v53, v60, v61
	s_waitcnt lgkmcnt(1)
	v_cvt_pk_bf16_f32 v54, v62, v63
	s_waitcnt lgkmcnt(0)
	v_cvt_pk_bf16_f32 v55, v64, v65
	ds_read2_b32 v[58:59], v31 offset1:1
	ds_read2_b32 v[60:61], v32 offset1:1
	ds_read2_b32 v[62:63], v33 offset1:1
	ds_read2_b32 v[64:65], v34 offset1:1
	v_lshlrev_b64 v[56:57], 11, v[56:57]
	v_lshl_add_u64 v[56:57], v[10:11], 0, v[56:57]
	global_store_dwordx4 v[56:57], v[52:55], off nt
	v_or_b32_e32 v56, s8, v17
	v_mov_b32_e32 v57, v3
	s_waitcnt lgkmcnt(3)
	v_cvt_pk_bf16_f32 v52, v58, v59
	s_waitcnt lgkmcnt(2)
	v_cvt_pk_bf16_f32 v53, v60, v61
	s_waitcnt lgkmcnt(1)
	v_cvt_pk_bf16_f32 v54, v62, v63
	s_waitcnt lgkmcnt(0)
	v_cvt_pk_bf16_f32 v55, v64, v65
	ds_read2_b32 v[58:59], v35 offset1:1
	ds_read2_b32 v[60:61], v36 offset1:1
	ds_read2_b32 v[62:63], v37 offset1:1
	ds_read2_b32 v[64:65], v38 offset1:1
	v_lshlrev_b64 v[56:57], 11, v[56:57]
	v_lshl_add_u64 v[56:57], v[10:11], 0, v[56:57]
	global_store_dwordx4 v[56:57], v[52:55], off nt
	v_or_b32_e32 v56, s8, v18
	v_mov_b32_e32 v57, v3
	s_waitcnt lgkmcnt(3)
	v_cvt_pk_bf16_f32 v52, v58, v59
	s_waitcnt lgkmcnt(2)
	v_cvt_pk_bf16_f32 v53, v60, v61
	s_waitcnt lgkmcnt(1)
	v_cvt_pk_bf16_f32 v54, v62, v63
	s_waitcnt lgkmcnt(0)
	v_cvt_pk_bf16_f32 v55, v64, v65
	ds_read2_b32 v[58:59], v39 offset1:1
	ds_read2_b32 v[60:61], v40 offset1:1
	ds_read2_b32 v[62:63], v41 offset1:1
	ds_read2_b32 v[64:65], v42 offset1:1
	v_lshlrev_b64 v[56:57], 11, v[56:57]
	v_lshl_add_u64 v[56:57], v[10:11], 0, v[56:57]
	global_store_dwordx4 v[56:57], v[52:55], off nt
	v_or_b32_e32 v56, s8, v19
	v_mov_b32_e32 v57, v3
	s_waitcnt lgkmcnt(3)
	v_cvt_pk_bf16_f32 v52, v58, v59
	s_waitcnt lgkmcnt(2)
	v_cvt_pk_bf16_f32 v53, v60, v61
	s_waitcnt lgkmcnt(1)
	v_cvt_pk_bf16_f32 v54, v62, v63
	s_waitcnt lgkmcnt(0)
	v_cvt_pk_bf16_f32 v55, v64, v65
	ds_read2_b32 v[58:59], v43 offset1:1
	ds_read2_b32 v[60:61], v44 offset1:1
	ds_read2_b32 v[62:63], v45 offset1:1
	ds_read2_b32 v[64:65], v46 offset1:1
	v_lshlrev_b64 v[56:57], 11, v[56:57]
	v_lshl_add_u64 v[56:57], v[10:11], 0, v[56:57]
	global_store_dwordx4 v[56:57], v[52:55], off nt
	v_or_b32_e32 v56, s8, v20
	v_mov_b32_e32 v57, v3
	s_waitcnt lgkmcnt(3)
	v_cvt_pk_bf16_f32 v52, v58, v59
	s_waitcnt lgkmcnt(2)
	v_cvt_pk_bf16_f32 v53, v60, v61
	s_waitcnt lgkmcnt(1)
	v_cvt_pk_bf16_f32 v54, v62, v63
	s_waitcnt lgkmcnt(0)
	v_cvt_pk_bf16_f32 v55, v64, v65
	ds_read2_b32 v[58:59], v47 offset1:1
	ds_read2_b32 v[60:61], v48 offset1:1
	ds_read2_b32 v[62:63], v49 offset1:1
	ds_read2_b32 v[64:65], v50 offset1:1
	v_lshlrev_b64 v[56:57], 11, v[56:57]
	v_lshl_add_u64 v[56:57], v[10:11], 0, v[56:57]
	global_store_dwordx4 v[56:57], v[52:55], off nt
	v_or_b32_e32 v56, s8, v21
	v_mov_b32_e32 v57, v3
	v_lshlrev_b64 v[56:57], 11, v[56:57]
	s_waitcnt lgkmcnt(3)
	v_cvt_pk_bf16_f32 v52, v58, v59
	s_waitcnt lgkmcnt(2)
	v_cvt_pk_bf16_f32 v53, v60, v61
	s_waitcnt lgkmcnt(1)
	v_cvt_pk_bf16_f32 v54, v62, v63
	s_waitcnt lgkmcnt(0)
	v_cvt_pk_bf16_f32 v55, v64, v65
	v_lshl_add_u64 v[10:11], v[10:11], 0, v[56:57]
	global_store_dwordx4 v[10:11], v[52:55], off nt
	s_waitcnt lgkmcnt(0)

.LBB0_53:
	s_andn2_b64 vcc, exec, s[14:15]
	s_cbranch_vccnz .LBB0_55
	s_load_dwordx2 s[14:15], s[28:29], 0xa0
	s_lshl_b64 s[44:45], s[12:13], 22
	s_mul_i32 s8, s12, 0xfffe6600
	v_mov_b32_e32 v53, v3
	s_waitcnt lgkmcnt(0)
	s_add_u32 s40, s14, s44
	s_addc_u32 s42, s15, s45
	s_add_i32 s8, s84, s8
	s_and_b32 s8, s8, 0x1fc0
	s_and_b32 s44, s85, 0x3c0
	s_addk_i32 s8, 0xee00
	s_lshl_b64 s[14:15], s[12:13], 21
	s_add_u32 s13, s22, s14
	s_addc_u32 s45, s23, s15
	s_lshl_b64 s[14:15], s[8:9], 2
	s_add_u32 s14, s40, s14
	v_or_b32_e32 v52, s44, v9
	s_addc_u32 s15, s42, s15
	v_lshl_add_u64 v[10:11], s[14:15], 0, v[2:3]
	v_lshlrev_b32_e32 v52, 12, v52
	v_lshl_add_u64 v[10:11], v[10:11], 0, v[52:53]
	v_add_co_u32_e32 v56, vcc, s30, v10
	s_lshl_b32 s14, s44, 1
	s_nop 0
	v_addc_co_u32_e32 v57, vcc, 0, v11, vcc
	v_add_co_u32_e32 v60, vcc, s31, v10
	global_load_dwordx4 v[52:55], v[10:11], off nt
	s_nop 0
	global_load_dwordx4 v[56:59], v[56:57], off nt
	v_addc_co_u32_e32 v61, vcc, 0, v11, vcc
	v_add_co_u32_e32 v64, vcc, s33, v10
	s_add_u32 s14, s13, s14
	s_nop 0
	v_addc_co_u32_e32 v65, vcc, 0, v11, vcc
	v_add_co_u32_e32 v68, vcc, s34, v10
	global_load_dwordx4 v[60:63], v[60:61], off nt
	s_nop 0
	global_load_dwordx4 v[64:67], v[64:65], off nt
	v_addc_co_u32_e32 v69, vcc, 0, v11, vcc
	v_add_co_u32_e32 v72, vcc, s35, v10
	s_addc_u32 s15, s45, 0
	s_nop 0
	v_addc_co_u32_e32 v73, vcc, 0, v11, vcc
	v_add_co_u32_e32 v76, vcc, s36, v10
	global_load_dwordx4 v[68:71], v[68:69], off nt
	s_nop 0
	global_load_dwordx4 v[72:75], v[72:73], off nt
	v_addc_co_u32_e32 v77, vcc, 0, v11, vcc
	v_add_co_u32_e32 v80, vcc, s37, v10
	s_nop 1
	v_addc_co_u32_e32 v81, vcc, 0, v11, vcc
	v_add_co_u32_e32 v84, vcc, s38, v10
	global_load_dwordx4 v[76:79], v[76:77], off nt
	s_nop 0
	global_load_dwordx4 v[80:83], v[80:81], off nt
	v_addc_co_u32_e32 v85, vcc, 0, v11, vcc
	v_add_co_u32_e32 v88, vcc, s39, v10
	s_nop 1
	v_addc_co_u32_e32 v89, vcc, 0, v11, vcc
	v_add_co_u32_e32 v92, vcc, s41, v10
	global_load_dwordx4 v[84:87], v[84:85], off nt
	s_nop 0
	global_load_dwordx4 v[88:91], v[88:89], off nt
	v_addc_co_u32_e32 v93, vcc, 0, v11, vcc
	v_add_co_u32_e32 v96, vcc, s43, v10
	s_nop 1
	v_addc_co_u32_e32 v97, vcc, 0, v11, vcc
	v_add_co_u32_e32 v100, vcc, s46, v10
	global_load_dwordx4 v[92:95], v[92:93], off nt
	s_nop 0
	global_load_dwordx4 v[96:99], v[96:97], off nt
	v_addc_co_u32_e32 v101, vcc, 0, v11, vcc
	v_add_co_u32_e32 v104, vcc, s47, v10
	s_nop 1
	v_addc_co_u32_e32 v105, vcc, 0, v11, vcc
	v_add_co_u32_e32 v108, vcc, s48, v10
	global_load_dwordx4 v[100:103], v[100:101], off nt
	s_nop 0
	global_load_dwordx4 v[104:107], v[104:105], off nt
	v_addc_co_u32_e32 v109, vcc, 0, v11, vcc
	v_add_co_u32_e32 v10, vcc, s49, v10
	s_nop 1
	v_addc_co_u32_e32 v11, vcc, 0, v11, vcc
	global_load_dwordx4 v[108:111], v[108:109], off nt
	s_nop 0
	global_load_dwordx4 v[112:115], v[10:11], off nt
	v_lshlrev_b32_e32 v10, 1, v4
	v_mov_b32_e32 v11, v3
	v_lshl_add_u64 v[10:11], s[14:15], 0, v[10:11]
	s_waitcnt vmcnt(14)
	ds_write2_b32 v12, v52, v56 offset1:4
	ds_write2_b32 v12, v53, v57 offset0:65 offset1:69
	ds_write2_b32 v12, v54, v58 offset0:130 offset1:134
	ds_write2_b32 v12, v55, v59 offset0:195 offset1:199
	s_waitcnt vmcnt(12)
	ds_write2_b32 v12, v60, v64 offset0:8 offset1:12
	ds_write2_b32 v12, v61, v65 offset0:73 offset1:77
	ds_write2_b32 v12, v62, v66 offset0:138 offset1:142
	ds_write2_b32 v12, v63, v67 offset0:203 offset1:207
	s_waitcnt vmcnt(10)
	ds_write2_b32 v12, v68, v72 offset0:16 offset1:20
	ds_write2_b32 v12, v69, v73 offset0:81 offset1:85
	ds_write2_b32 v12, v70, v74 offset0:146 offset1:150
	ds_write2_b32 v12, v71, v75 offset0:211 offset1:215
	s_waitcnt vmcnt(8)
	ds_write2_b32 v12, v76, v80 offset0:24 offset1:28
	ds_write2_b32 v12, v77, v81 offset0:89 offset1:93
	ds_write2_b32 v12, v78, v82 offset0:154 offset1:158
	ds_write2_b32 v12, v79, v83 offset0:219 offset1:223
	s_waitcnt vmcnt(6)
	ds_write2_b32 v12, v84, v88 offset0:32 offset1:36
	ds_write2_b32 v12, v85, v89 offset0:97 offset1:101
	ds_write2_b32 v12, v86, v90 offset0:162 offset1:166
	ds_write2_b32 v12, v87, v91 offset0:227 offset1:231
	s_waitcnt vmcnt(4)
	ds_write2_b32 v12, v92, v96 offset0:40 offset1:44
	ds_write2_b32 v12, v93, v97 offset0:105 offset1:109
	ds_write2_b32 v12, v94, v98 offset0:170 offset1:174
	ds_write2_b32 v12, v95, v99 offset0:235 offset1:239
	s_waitcnt vmcnt(2)
	ds_write2_b32 v12, v100, v104 offset0:48 offset1:52
	ds_write2_b32 v12, v101, v105 offset0:113 offset1:117
	ds_write2_b32 v12, v102, v106 offset0:178 offset1:182
	ds_write2_b32 v12, v103, v107 offset0:243 offset1:247
	s_waitcnt vmcnt(0)
	ds_write2_b32 v12, v108, v112 offset0:56 offset1:60
	ds_write2_b32 v12, v109, v113 offset0:121 offset1:125
	ds_write2_b32 v12, v110, v114 offset0:186 offset1:190
	ds_write2_b32 v12, v111, v115 offset0:251 offset1:255
	s_waitcnt lgkmcnt(0)
	ds_read2_b32 v[52:53], v14 offset1:1
	ds_read2_b32 v[54:55], v14 offset0:2 offset1:3
	ds_read2_b32 v[56:57], v14 offset0:4 offset1:5
	ds_read2_b32 v[58:59], v14 offset0:6 offset1:7
	s_waitcnt lgkmcnt(3)
	v_cvt_pk_bf16_f32 v52, v52, v53
	s_waitcnt lgkmcnt(2)
	v_cvt_pk_bf16_f32 v53, v54, v55
	s_waitcnt lgkmcnt(1)
	v_cvt_pk_bf16_f32 v54, v56, v57
	s_waitcnt lgkmcnt(0)
	v_cvt_pk_bf16_f32 v55, v58, v59
	ds_read2_b32 v[58:59], v26 offset1:1
	ds_read2_b32 v[60:61], v26 offset0:2 offset1:3
	ds_read2_b32 v[62:63], v26 offset0:4 offset1:5
	ds_read2_b32 v[64:65], v26 offset0:6 offset1:7
	v_or_b32_e32 v56, s8, v13
	v_mov_b32_e32 v57, v3
	v_lshlrev_b64 v[56:57], 11, v[56:57]
	v_lshl_add_u64 v[56:57], v[10:11], 0, v[56:57]
	global_store_dwordx4 v[56:57], v[52:55], off nt
	v_or_b32_e32 v56, s8, v15
	v_mov_b32_e32 v57, v3
	s_waitcnt lgkmcnt(3)
	v_cvt_pk_bf16_f32 v52, v58, v59
	s_waitcnt lgkmcnt(2)
	v_cvt_pk_bf16_f32 v53, v60, v61
	s_waitcnt lgkmcnt(1)
	v_cvt_pk_bf16_f32 v54, v62, v63
	s_waitcnt lgkmcnt(0)
	v_cvt_pk_bf16_f32 v55, v64, v65
	ds_read2_b32 v[58:59], v27 offset1:1
	ds_read2_b32 v[60:61], v28 offset1:1
	ds_read2_b32 v[62:63], v29 offset1:1
	ds_read2_b32 v[64:65], v30 offset1:1
	v_lshlrev_b64 v[56:57], 11, v[56:57]
	v_lshl_add_u64 v[56:57], v[10:11], 0, v[56:57]
	global_store_dwordx4 v[56:57], v[52:55], off nt
	v_or_b32_e32 v56, s8, v16
	v_mov_b32_e32 v57, v3
	s_waitcnt lgkmcnt(3)
	v_cvt_pk_bf16_f32 v52, v58, v59
	s_waitcnt lgkmcnt(2)
	v_cvt_pk_bf16_f32 v53, v60, v61
	s_waitcnt lgkmcnt(1)
	v_cvt_pk_bf16_f32 v54, v62, v63
	s_waitcnt lgkmcnt(0)
	v_cvt_pk_bf16_f32 v55, v64, v65
	ds_read2_b32 v[58:59], v31 offset1:1
	ds_read2_b32 v[60:61], v32 offset1:1
	ds_read2_b32 v[62:63], v33 offset1:1
	ds_read2_b32 v[64:65], v34 offset1:1
	v_lshlrev_b64 v[56:57], 11, v[56:57]
	v_lshl_add_u64 v[56:57], v[10:11], 0, v[56:57]
	global_store_dwordx4 v[56:57], v[52:55], off nt
	v_or_b32_e32 v56, s8, v17
	v_mov_b32_e32 v57, v3
	s_waitcnt lgkmcnt(3)
	v_cvt_pk_bf16_f32 v52, v58, v59
	s_waitcnt lgkmcnt(2)
	v_cvt_pk_bf16_f32 v53, v60, v61
	s_waitcnt lgkmcnt(1)
	v_cvt_pk_bf16_f32 v54, v62, v63
	s_waitcnt lgkmcnt(0)
	v_cvt_pk_bf16_f32 v55, v64, v65
	ds_read2_b32 v[58:59], v35 offset1:1
	ds_read2_b32 v[60:61], v36 offset1:1
	ds_read2_b32 v[62:63], v37 offset1:1
	ds_read2_b32 v[64:65], v38 offset1:1
	v_lshlrev_b64 v[56:57], 11, v[56:57]
	v_lshl_add_u64 v[56:57], v[10:11], 0, v[56:57]
	global_store_dwordx4 v[56:57], v[52:55], off nt
	v_or_b32_e32 v56, s8, v18
	v_mov_b32_e32 v57, v3
	s_waitcnt lgkmcnt(3)
	v_cvt_pk_bf16_f32 v52, v58, v59
	s_waitcnt lgkmcnt(2)
	v_cvt_pk_bf16_f32 v53, v60, v61
	s_waitcnt lgkmcnt(1)
	v_cvt_pk_bf16_f32 v54, v62, v63
	s_waitcnt lgkmcnt(0)
	v_cvt_pk_bf16_f32 v55, v64, v65
	ds_read2_b32 v[58:59], v39 offset1:1
	ds_read2_b32 v[60:61], v40 offset1:1
	ds_read2_b32 v[62:63], v41 offset1:1
	ds_read2_b32 v[64:65], v42 offset1:1
	v_lshlrev_b64 v[56:57], 11, v[56:57]
	v_lshl_add_u64 v[56:57], v[10:11], 0, v[56:57]
	global_store_dwordx4 v[56:57], v[52:55], off nt
	v_or_b32_e32 v56, s8, v19
	v_mov_b32_e32 v57, v3
	s_waitcnt lgkmcnt(3)
	v_cvt_pk_bf16_f32 v52, v58, v59
	s_waitcnt lgkmcnt(2)
	v_cvt_pk_bf16_f32 v53, v60, v61
	s_waitcnt lgkmcnt(1)
	v_cvt_pk_bf16_f32 v54, v62, v63
	s_waitcnt lgkmcnt(0)
	v_cvt_pk_bf16_f32 v55, v64, v65
	ds_read2_b32 v[58:59], v43 offset1:1
	ds_read2_b32 v[60:61], v44 offset1:1
	ds_read2_b32 v[62:63], v45 offset1:1
	ds_read2_b32 v[64:65], v46 offset1:1
	v_lshlrev_b64 v[56:57], 11, v[56:57]
	v_lshl_add_u64 v[56:57], v[10:11], 0, v[56:57]
	global_store_dwordx4 v[56:57], v[52:55], off nt
	v_or_b32_e32 v56, s8, v20
	v_mov_b32_e32 v57, v3
	s_waitcnt lgkmcnt(3)
	v_cvt_pk_bf16_f32 v52, v58, v59
	s_waitcnt lgkmcnt(2)
	v_cvt_pk_bf16_f32 v53, v60, v61
	s_waitcnt lgkmcnt(1)
	v_cvt_pk_bf16_f32 v54, v62, v63
	s_waitcnt lgkmcnt(0)
	v_cvt_pk_bf16_f32 v55, v64, v65
	ds_read2_b32 v[58:59], v47 offset1:1
	ds_read2_b32 v[60:61], v48 offset1:1
	ds_read2_b32 v[62:63], v49 offset1:1
	ds_read2_b32 v[64:65], v50 offset1:1
	v_lshlrev_b64 v[56:57], 11, v[56:57]
	v_lshl_add_u64 v[56:57], v[10:11], 0, v[56:57]
	global_store_dwordx4 v[56:57], v[52:55], off nt
	v_or_b32_e32 v56, s8, v21
	v_mov_b32_e32 v57, v3
	v_lshlrev_b64 v[56:57], 11, v[56:57]
	s_waitcnt lgkmcnt(3)
	v_cvt_pk_bf16_f32 v52, v58, v59
	s_waitcnt lgkmcnt(2)
	v_cvt_pk_bf16_f32 v53, v60, v61
	s_waitcnt lgkmcnt(1)
	v_cvt_pk_bf16_f32 v54, v62, v63
	s_waitcnt lgkmcnt(0)
	v_cvt_pk_bf16_f32 v55, v64, v65
	v_lshl_add_u64 v[10:11], v[10:11], 0, v[56:57]
	global_store_dwordx4 v[10:11], v[52:55], off nt
	s_waitcnt lgkmcnt(0)

.LBB0_56:
	s_andn2_b64 vcc, exec, s[14:15]
	s_cbranch_vccnz .LBB0_58
	s_mul_i32 s13, s12, 0x280000
	s_mul_hi_i32 s8, s12, 0x280000
	s_add_u32 s13, s0, s13
	s_addc_u32 s40, s1, s8
	s_mul_i32 s8, s12, 0xfffe6600
	s_add_i32 s8, s84, s8
	s_and_b32 s14, s8, 0x1fc0
	s_and_b32 s42, s85, 0x3c0
	s_add_i32 s8, s14, 0xfffff100
	s_lshl_b32 s14, s14, 2
	v_or_b32_e32 v52, s42, v9
	s_add_u32 s14, s88, s14
	s_addc_u32 s15, s89, 0
	v_mul_u32_u24_e32 v52, 0x1300, v52
	v_lshl_add_u64 v[10:11], s[14:15], 0, v[2:3]
	v_lshlrev_b32_e32 v52, 2, v52
	v_mov_b32_e32 v53, v3
	v_lshl_add_u64 v[10:11], v[10:11], 0, v[52:53]
	s_movk_i32 s14, 0xd000
	v_add_co_u32_e32 v52, vcc, s14, v10
	s_mov_b32 s14, 0x23000
	s_nop 0
	v_addc_co_u32_e32 v53, vcc, -1, v11, vcc
	v_add_co_u32_e32 v56, vcc, s34, v10
	s_nop 1
	v_addc_co_u32_e32 v57, vcc, 0, v11, vcc
	v_add_co_u32_e32 v60, vcc, s14, v10
	s_mov_b32 s14, 0x36000
	s_nop 0
	v_addc_co_u32_e32 v61, vcc, 0, v11, vcc
	v_add_co_u32_e32 v64, vcc, s14, v10
	s_mov_b32 s14, 0x49000
	s_nop 0
	v_addc_co_u32_e32 v65, vcc, 0, v11, vcc
	v_add_co_u32_e32 v68, vcc, s14, v10
	s_mov_b32 s14, 0x5c000
	s_nop 0
	v_addc_co_u32_e32 v69, vcc, 0, v11, vcc
	v_add_co_u32_e32 v72, vcc, s14, v10
	s_mov_b32 s14, 0x6f000
	s_nop 0
	v_addc_co_u32_e32 v73, vcc, 0, v11, vcc
	v_add_co_u32_e32 v76, vcc, s14, v10
	s_mov_b32 s14, 0x82000
	s_nop 0
	v_addc_co_u32_e32 v77, vcc, 0, v11, vcc
	v_add_co_u32_e32 v80, vcc, s14, v10
	s_mov_b32 s14, 0x95000
	s_nop 0
	v_addc_co_u32_e32 v81, vcc, 0, v11, vcc
	v_add_co_u32_e32 v84, vcc, s14, v10
	s_mov_b32 s14, 0xa8000
	s_nop 0
	v_addc_co_u32_e32 v85, vcc, 0, v11, vcc
	v_add_co_u32_e32 v88, vcc, s14, v10
	s_mov_b32 s14, 0xbb000
	s_nop 0
	v_addc_co_u32_e32 v89, vcc, 0, v11, vcc
	v_add_co_u32_e32 v92, vcc, s14, v10
	s_mov_b32 s14, 0xce000
	s_nop 0
	v_addc_co_u32_e32 v93, vcc, 0, v11, vcc
	v_add_co_u32_e32 v96, vcc, s14, v10
	s_mov_b32 s14, 0xe1000
	s_nop 0
	v_addc_co_u32_e32 v97, vcc, 0, v11, vcc
	v_add_co_u32_e32 v100, vcc, s14, v10
	s_mov_b32 s14, 0xf4000
	s_nop 0
	v_addc_co_u32_e32 v101, vcc, 0, v11, vcc
	v_add_co_u32_e32 v104, vcc, s14, v10
	global_load_dwordx4 v[52:55], v[52:53], off nt
	s_nop 0
	global_load_dwordx4 v[56:59], v[56:57], off nt
	v_addc_co_u32_e32 v105, vcc, 0, v11, vcc
	v_add_co_u32_e32 v108, vcc, s52, v10
	global_load_dwordx4 v[60:63], v[60:61], off nt
	s_nop 0
	global_load_dwordx4 v[64:67], v[64:65], off nt
	v_addc_co_u32_e32 v109, vcc, 0, v11, vcc
	v_add_co_u32_e32 v10, vcc, s53, v10
	global_load_dwordx4 v[68:71], v[68:69], off nt
	s_nop 0
	global_load_dwordx4 v[72:75], v[72:73], off nt
	s_nop 0
	global_load_dwordx4 v[76:79], v[76:77], off nt
	s_nop 0
	global_load_dwordx4 v[80:83], v[80:81], off nt
	s_nop 0
	global_load_dwordx4 v[84:87], v[84:85], off nt
	s_nop 0
	global_load_dwordx4 v[88:91], v[88:89], off nt
	s_nop 0
	global_load_dwordx4 v[92:95], v[92:93], off nt
	s_nop 0
	global_load_dwordx4 v[96:99], v[96:97], off nt
	s_nop 0
	global_load_dwordx4 v[100:103], v[100:101], off nt
	s_nop 0
	global_load_dwordx4 v[104:107], v[104:105], off nt
	v_addc_co_u32_e32 v11, vcc, 0, v11, vcc
	global_load_dwordx4 v[108:111], v[108:109], off nt
	s_nop 0
	global_load_dwordx4 v[112:115], v[10:11], off nt
	s_lshl_b32 s14, s42, 1
	s_add_u32 s14, s13, s14
	s_addc_u32 s15, s40, 0
	v_lshlrev_b32_e32 v10, 1, v4
	v_mov_b32_e32 v11, v3
	v_lshl_add_u64 v[10:11], s[14:15], 0, v[10:11]
	s_waitcnt vmcnt(14)
	ds_write2_b32 v12, v52, v56 offset1:4
	ds_write2_b32 v12, v53, v57 offset0:65 offset1:69
	ds_write2_b32 v12, v54, v58 offset0:130 offset1:134
	ds_write2_b32 v12, v55, v59 offset0:195 offset1:199
	s_waitcnt vmcnt(12)
	ds_write2_b32 v12, v60, v64 offset0:8 offset1:12
	ds_write2_b32 v12, v61, v65 offset0:73 offset1:77
	ds_write2_b32 v12, v62, v66 offset0:138 offset1:142
	ds_write2_b32 v12, v63, v67 offset0:203 offset1:207
	s_waitcnt vmcnt(10)
	ds_write2_b32 v12, v68, v72 offset0:16 offset1:20
	ds_write2_b32 v12, v69, v73 offset0:81 offset1:85
	ds_write2_b32 v12, v70, v74 offset0:146 offset1:150
	ds_write2_b32 v12, v71, v75 offset0:211 offset1:215
	s_waitcnt vmcnt(8)
	ds_write2_b32 v12, v76, v80 offset0:24 offset1:28
	ds_write2_b32 v12, v77, v81 offset0:89 offset1:93
	ds_write2_b32 v12, v78, v82 offset0:154 offset1:158
	ds_write2_b32 v12, v79, v83 offset0:219 offset1:223
	s_waitcnt vmcnt(6)
	ds_write2_b32 v12, v84, v88 offset0:32 offset1:36
	ds_write2_b32 v12, v85, v89 offset0:97 offset1:101
	ds_write2_b32 v12, v86, v90 offset0:162 offset1:166
	ds_write2_b32 v12, v87, v91 offset0:227 offset1:231
	s_waitcnt vmcnt(4)
	ds_write2_b32 v12, v92, v96 offset0:40 offset1:44
	ds_write2_b32 v12, v93, v97 offset0:105 offset1:109
	ds_write2_b32 v12, v94, v98 offset0:170 offset1:174
	ds_write2_b32 v12, v95, v99 offset0:235 offset1:239
	s_waitcnt vmcnt(2)
	ds_write2_b32 v12, v100, v104 offset0:48 offset1:52
	ds_write2_b32 v12, v101, v105 offset0:113 offset1:117
	ds_write2_b32 v12, v102, v106 offset0:178 offset1:182
	ds_write2_b32 v12, v103, v107 offset0:243 offset1:247
	s_waitcnt vmcnt(0)
	ds_write2_b32 v12, v108, v112 offset0:56 offset1:60
	ds_write2_b32 v12, v109, v113 offset0:121 offset1:125
	ds_write2_b32 v12, v110, v114 offset0:186 offset1:190
	ds_write2_b32 v12, v111, v115 offset0:251 offset1:255
	s_waitcnt lgkmcnt(0)
	ds_read2_b32 v[52:53], v14 offset1:1
	ds_read2_b32 v[54:55], v14 offset0:2 offset1:3
	ds_read2_b32 v[56:57], v14 offset0:4 offset1:5
	ds_read2_b32 v[58:59], v14 offset0:6 offset1:7
	s_waitcnt lgkmcnt(3)
	v_cvt_pk_bf16_f32 v52, v52, v53
	s_waitcnt lgkmcnt(2)
	v_cvt_pk_bf16_f32 v53, v54, v55
	s_waitcnt lgkmcnt(1)
	v_cvt_pk_bf16_f32 v54, v56, v57
	s_waitcnt lgkmcnt(0)
	v_cvt_pk_bf16_f32 v55, v58, v59
	ds_read2_b32 v[58:59], v26 offset1:1
	ds_read2_b32 v[60:61], v26 offset0:2 offset1:3
	ds_read2_b32 v[62:63], v26 offset0:4 offset1:5
	ds_read2_b32 v[64:65], v26 offset0:6 offset1:7
	v_or_b32_e32 v56, s8, v13
	v_mov_b32_e32 v57, v3
	v_lshlrev_b64 v[56:57], 11, v[56:57]
	v_lshl_add_u64 v[56:57], v[10:11], 0, v[56:57]
	global_store_dwordx4 v[56:57], v[52:55], off nt
	v_or_b32_e32 v56, s8, v15
	v_mov_b32_e32 v57, v3
	s_waitcnt lgkmcnt(3)
	v_cvt_pk_bf16_f32 v52, v58, v59
	s_waitcnt lgkmcnt(2)
	v_cvt_pk_bf16_f32 v53, v60, v61
	s_waitcnt lgkmcnt(1)
	v_cvt_pk_bf16_f32 v54, v62, v63
	s_waitcnt lgkmcnt(0)
	v_cvt_pk_bf16_f32 v55, v64, v65
	ds_read2_b32 v[58:59], v27 offset1:1
	ds_read2_b32 v[60:61], v28 offset1:1
	ds_read2_b32 v[62:63], v29 offset1:1
	ds_read2_b32 v[64:65], v30 offset1:1
	v_lshlrev_b64 v[56:57], 11, v[56:57]
	v_lshl_add_u64 v[56:57], v[10:11], 0, v[56:57]
	global_store_dwordx4 v[56:57], v[52:55], off nt
	v_or_b32_e32 v56, s8, v16
	v_mov_b32_e32 v57, v3
	s_waitcnt lgkmcnt(3)
	v_cvt_pk_bf16_f32 v52, v58, v59
	s_waitcnt lgkmcnt(2)
	v_cvt_pk_bf16_f32 v53, v60, v61
	s_waitcnt lgkmcnt(1)
	v_cvt_pk_bf16_f32 v54, v62, v63
	s_waitcnt lgkmcnt(0)
	v_cvt_pk_bf16_f32 v55, v64, v65
	ds_read2_b32 v[58:59], v31 offset1:1
	ds_read2_b32 v[60:61], v32 offset1:1
	ds_read2_b32 v[62:63], v33 offset1:1
	ds_read2_b32 v[64:65], v34 offset1:1
	v_lshlrev_b64 v[56:57], 11, v[56:57]
	v_lshl_add_u64 v[56:57], v[10:11], 0, v[56:57]
	global_store_dwordx4 v[56:57], v[52:55], off nt
	v_or_b32_e32 v56, s8, v17
	v_mov_b32_e32 v57, v3
	s_waitcnt lgkmcnt(3)
	v_cvt_pk_bf16_f32 v52, v58, v59
	s_waitcnt lgkmcnt(2)
	v_cvt_pk_bf16_f32 v53, v60, v61
	s_waitcnt lgkmcnt(1)
	v_cvt_pk_bf16_f32 v54, v62, v63
	s_waitcnt lgkmcnt(0)
	v_cvt_pk_bf16_f32 v55, v64, v65
	ds_read2_b32 v[58:59], v35 offset1:1
	ds_read2_b32 v[60:61], v36 offset1:1
	ds_read2_b32 v[62:63], v37 offset1:1
	ds_read2_b32 v[64:65], v38 offset1:1
	v_lshlrev_b64 v[56:57], 11, v[56:57]
	v_lshl_add_u64 v[56:57], v[10:11], 0, v[56:57]
	global_store_dwordx4 v[56:57], v[52:55], off nt
	v_or_b32_e32 v56, s8, v18
	v_mov_b32_e32 v57, v3
	s_waitcnt lgkmcnt(3)
	v_cvt_pk_bf16_f32 v52, v58, v59
	s_waitcnt lgkmcnt(2)
	v_cvt_pk_bf16_f32 v53, v60, v61
	s_waitcnt lgkmcnt(1)
	v_cvt_pk_bf16_f32 v54, v62, v63
	s_waitcnt lgkmcnt(0)
	v_cvt_pk_bf16_f32 v55, v64, v65
	ds_read2_b32 v[58:59], v39 offset1:1
	ds_read2_b32 v[60:61], v40 offset1:1
	ds_read2_b32 v[62:63], v41 offset1:1
	ds_read2_b32 v[64:65], v42 offset1:1
	v_lshlrev_b64 v[56:57], 11, v[56:57]
	v_lshl_add_u64 v[56:57], v[10:11], 0, v[56:57]
	global_store_dwordx4 v[56:57], v[52:55], off nt
	v_or_b32_e32 v56, s8, v19
	v_mov_b32_e32 v57, v3
	s_waitcnt lgkmcnt(3)
	v_cvt_pk_bf16_f32 v52, v58, v59
	s_waitcnt lgkmcnt(2)
	v_cvt_pk_bf16_f32 v53, v60, v61
	s_waitcnt lgkmcnt(1)
	v_cvt_pk_bf16_f32 v54, v62, v63
	s_waitcnt lgkmcnt(0)
	v_cvt_pk_bf16_f32 v55, v64, v65
	ds_read2_b32 v[58:59], v43 offset1:1
	ds_read2_b32 v[60:61], v44 offset1:1
	ds_read2_b32 v[62:63], v45 offset1:1
	ds_read2_b32 v[64:65], v46 offset1:1
	v_lshlrev_b64 v[56:57], 11, v[56:57]
	v_lshl_add_u64 v[56:57], v[10:11], 0, v[56:57]
	global_store_dwordx4 v[56:57], v[52:55], off nt
	v_or_b32_e32 v56, s8, v20
	v_mov_b32_e32 v57, v3
	s_waitcnt lgkmcnt(3)
	v_cvt_pk_bf16_f32 v52, v58, v59
	s_waitcnt lgkmcnt(2)
	v_cvt_pk_bf16_f32 v53, v60, v61
	s_waitcnt lgkmcnt(1)
	v_cvt_pk_bf16_f32 v54, v62, v63
	s_waitcnt lgkmcnt(0)
	v_cvt_pk_bf16_f32 v55, v64, v65
	ds_read2_b32 v[58:59], v47 offset1:1
	ds_read2_b32 v[60:61], v48 offset1:1
	ds_read2_b32 v[62:63], v49 offset1:1
	ds_read2_b32 v[64:65], v50 offset1:1
	v_lshlrev_b64 v[56:57], 11, v[56:57]
	v_lshl_add_u64 v[56:57], v[10:11], 0, v[56:57]
	global_store_dwordx4 v[56:57], v[52:55], off nt
	v_or_b32_e32 v56, s8, v21
	v_mov_b32_e32 v57, v3
	v_lshlrev_b64 v[56:57], 11, v[56:57]
	s_waitcnt lgkmcnt(3)
	v_cvt_pk_bf16_f32 v52, v58, v59
	s_waitcnt lgkmcnt(2)
	v_cvt_pk_bf16_f32 v53, v60, v61
	s_waitcnt lgkmcnt(1)
	v_cvt_pk_bf16_f32 v54, v62, v63
	s_waitcnt lgkmcnt(0)
	v_cvt_pk_bf16_f32 v55, v64, v65
	v_lshl_add_u64 v[10:11], v[10:11], 0, v[56:57]
	global_store_dwordx4 v[10:11], v[52:55], off nt
	s_waitcnt lgkmcnt(0)

.LBB0_59:
	s_andn2_b64 vcc, exec, s[14:15]
	s_cbranch_vccnz .LBB0_61
	s_mul_i32 s8, s12, 0xfffe6600
	s_add_i32 s8, s84, s8
	s_and_b32 s14, s8, 0xfc0
	s_and_b32 s13, s85, 0x3c0
	s_add_i32 s8, s14, 0xfffffd00
	s_mul_i32 s40, s12, 0x300000
	s_mul_hi_i32 s15, s12, 0x300000
	s_add_u32 s40, s24, s40
	s_addc_u32 s42, s25, s15
	s_lshl_b32 s14, s14, 2
	v_or_b32_e32 v52, s13, v9
	s_add_u32 s14, s88, s14
	s_addc_u32 s15, s89, 0
	v_mul_u32_u24_e32 v52, 0x1300, v52
	v_lshl_add_u64 v[10:11], s[14:15], 0, v[2:3]
	v_lshlrev_b32_e32 v52, 2, v52
	v_mov_b32_e32 v53, v3
	v_lshl_add_u64 v[10:11], v[10:11], 0, v[52:53]
	v_add_co_u32_e32 v52, vcc, s54, v10
	s_add_u32 s14, s40, s13
	s_nop 0
	v_addc_co_u32_e32 v53, vcc, 0, v11, vcc
	v_add_co_u32_e32 v56, vcc, s35, v10
	s_addc_u32 s15, s42, 0
	s_nop 0
	v_addc_co_u32_e32 v57, vcc, 0, v11, vcc
	v_add_co_u32_e32 v60, vcc, s55, v10
	global_load_dwordx4 v[52:55], v[52:53], off nt
	s_nop 0
	global_load_dwordx4 v[56:59], v[56:57], off nt
	v_addc_co_u32_e32 v61, vcc, 0, v11, vcc
	v_add_co_u32_e32 v64, vcc, s56, v10
	s_nop 1
	v_addc_co_u32_e32 v65, vcc, 0, v11, vcc
	v_add_co_u32_e32 v68, vcc, s57, v10
	global_load_dwordx4 v[60:63], v[60:61], off nt
	s_nop 0
	global_load_dwordx4 v[64:67], v[64:65], off nt
	v_addc_co_u32_e32 v69, vcc, 0, v11, vcc
	v_add_co_u32_e32 v72, vcc, s51, v10
	s_nop 1
	v_addc_co_u32_e32 v73, vcc, 0, v11, vcc
	v_add_co_u32_e32 v76, vcc, s58, v10
	global_load_dwordx4 v[68:71], v[68:69], off nt
	s_nop 0
	global_load_dwordx4 v[72:75], v[72:73], off nt
	v_addc_co_u32_e32 v77, vcc, 0, v11, vcc
	v_add_co_u32_e32 v80, vcc, s59, v10
	s_nop 1
	v_addc_co_u32_e32 v81, vcc, 0, v11, vcc
	v_add_co_u32_e32 v84, vcc, s60, v10
	s_nop 1
	v_addc_co_u32_e32 v85, vcc, 0, v11, vcc
	v_add_co_u32_e32 v88, vcc, s61, v10
	s_nop 1
	v_addc_co_u32_e32 v89, vcc, 0, v11, vcc
	v_add_co_u32_e32 v92, vcc, s62, v10
	s_nop 1
	v_addc_co_u32_e32 v93, vcc, 0, v11, vcc
	v_add_co_u32_e32 v96, vcc, s63, v10
	s_nop 1
	v_addc_co_u32_e32 v97, vcc, 0, v11, vcc
	v_add_co_u32_e32 v100, vcc, s64, v10
	s_nop 1
	v_addc_co_u32_e32 v101, vcc, 0, v11, vcc
	v_add_co_u32_e32 v104, vcc, s65, v10
	s_nop 1
	v_addc_co_u32_e32 v105, vcc, 0, v11, vcc
	v_add_co_u32_e32 v108, vcc, s66, v10
	global_load_dwordx4 v[76:79], v[76:77], off nt
	s_nop 0
	global_load_dwordx4 v[80:83], v[80:81], off nt
	s_nop 0
	global_load_dwordx4 v[84:87], v[84:85], off nt
	s_nop 0
	global_load_dwordx4 v[88:91], v[88:89], off nt
	s_nop 0
	global_load_dwordx4 v[92:95], v[92:93], off nt
	s_nop 0
	global_load_dwordx4 v[96:99], v[96:97], off nt
	s_nop 0
	global_load_dwordx4 v[100:103], v[100:101], off nt
	s_nop 0
	global_load_dwordx4 v[104:107], v[104:105], off nt
	v_addc_co_u32_e32 v109, vcc, 0, v11, vcc
	v_add_co_u32_e32 v10, vcc, s67, v10
	s_nop 1
	v_addc_co_u32_e32 v11, vcc, 0, v11, vcc
	global_load_dwordx4 v[108:111], v[108:109], off nt
	s_nop 0
	global_load_dwordx4 v[112:115], v[10:11], off nt
	v_lshl_add_u64 v[10:11], s[14:15], 0, v[4:5]
	s_waitcnt vmcnt(14)
	ds_write2_b32 v12, v52, v56 offset1:4
	ds_write2_b32 v12, v53, v57 offset0:65 offset1:69
	ds_write2_b32 v12, v54, v58 offset0:130 offset1:134
	ds_write2_b32 v12, v55, v59 offset0:195 offset1:199
	s_waitcnt vmcnt(12)
	ds_write2_b32 v12, v60, v64 offset0:8 offset1:12
	ds_write2_b32 v12, v61, v65 offset0:73 offset1:77
	ds_write2_b32 v12, v62, v66 offset0:138 offset1:142
	ds_write2_b32 v12, v63, v67 offset0:203 offset1:207
	s_waitcnt vmcnt(10)
	ds_write2_b32 v12, v68, v72 offset0:16 offset1:20
	ds_write2_b32 v12, v69, v73 offset0:81 offset1:85
	ds_write2_b32 v12, v70, v74 offset0:146 offset1:150
	ds_write2_b32 v12, v71, v75 offset0:211 offset1:215
	s_waitcnt vmcnt(8)
	ds_write2_b32 v12, v76, v80 offset0:24 offset1:28
	ds_write2_b32 v12, v77, v81 offset0:89 offset1:93
	ds_write2_b32 v12, v78, v82 offset0:154 offset1:158
	ds_write2_b32 v12, v79, v83 offset0:219 offset1:223
	s_waitcnt vmcnt(6)
	ds_write2_b32 v12, v84, v88 offset0:32 offset1:36
	ds_write2_b32 v12, v85, v89 offset0:97 offset1:101
	ds_write2_b32 v12, v86, v90 offset0:162 offset1:166
	ds_write2_b32 v12, v87, v91 offset0:227 offset1:231
	s_waitcnt vmcnt(4)
	ds_write2_b32 v12, v92, v96 offset0:40 offset1:44
	ds_write2_b32 v12, v93, v97 offset0:105 offset1:109
	ds_write2_b32 v12, v94, v98 offset0:170 offset1:174
	ds_write2_b32 v12, v95, v99 offset0:235 offset1:239
	s_waitcnt vmcnt(2)
	ds_write2_b32 v12, v100, v104 offset0:48 offset1:52
	ds_write2_b32 v12, v101, v105 offset0:113 offset1:117
	ds_write2_b32 v12, v102, v106 offset0:178 offset1:182
	ds_write2_b32 v12, v103, v107 offset0:243 offset1:247
	s_waitcnt vmcnt(0)
	ds_write2_b32 v12, v108, v112 offset0:56 offset1:60
	ds_write2_b32 v12, v109, v113 offset0:121 offset1:125
	ds_write2_b32 v12, v110, v114 offset0:186 offset1:190
	ds_write2_b32 v12, v111, v115 offset0:251 offset1:255
	s_waitcnt lgkmcnt(0)
	ds_read2_b32 v[52:53], v14 offset1:1
	ds_read2_b32 v[54:55], v14 offset0:2 offset1:3
	ds_read2_b32 v[56:57], v14 offset0:4 offset1:5
	ds_read2_b32 v[58:59], v14 offset0:6 offset1:7
	s_waitcnt lgkmcnt(2)
	v_mul_f32_e32 v54, 0x42800000, v54
	v_mul_f32_e32 v52, 0x42800000, v52
	v_mul_f32_e32 v53, 0x42800000, v53
	v_med3_f32 v60, v52, s50, v51
	v_med3_f32 v53, v53, s50, v51
	v_mov_b32_e32 v52, v3
	v_cvt_pk_fp8_f32 v52, v60, v53
	v_mul_f32_e32 v53, 0x42800000, v55
	v_med3_f32 v54, v54, s50, v51
	v_med3_f32 v53, v53, s50, v51
	v_cvt_pk_fp8_f32 v52, v54, v53 op_sel:[0,0,1]
	s_waitcnt lgkmcnt(1)
	v_mul_f32_e32 v53, 0x42800000, v56
	v_mul_f32_e32 v54, 0x42800000, v57
	v_med3_f32 v56, v53, s50, v51
	v_med3_f32 v54, v54, s50, v51
	v_mov_b32_e32 v53, v3
	v_cvt_pk_fp8_f32 v53, v56, v54
	s_waitcnt lgkmcnt(0)
	v_mul_f32_e32 v55, 0x42800000, v58
	v_mul_f32_e32 v54, 0x42800000, v59
	v_med3_f32 v55, v55, s50, v51
	v_med3_f32 v54, v54, s50, v51
	v_cvt_pk_fp8_f32 v53, v55, v54 op_sel:[0,0,1]
	v_or_b32_e32 v54, s8, v13
	v_mov_b32_e32 v55, v3
	v_lshlrev_b64 v[54:55], 10, v[54:55]
	ds_read2_b32 v[56:57], v26 offset1:1
	v_lshl_add_u64 v[54:55], v[10:11], 0, v[54:55]
	global_store_dwordx2 v[54:55], v[52:53], off nt
	ds_read2_b32 v[52:53], v26 offset0:2 offset1:3
	ds_read2_b32 v[54:55], v26 offset0:4 offset1:5
	ds_read2_b32 v[58:59], v26 offset0:6 offset1:7
	s_waitcnt lgkmcnt(3)
	v_mul_f32_e32 v56, 0x42800000, v56
	v_mul_f32_e32 v57, 0x42800000, v57
	s_waitcnt lgkmcnt(2)
	v_mul_f32_e32 v60, 0x42800000, v52
	v_med3_f32 v56, v56, s50, v51
	v_med3_f32 v57, v57, s50, v51
	v_mov_b32_e32 v52, v3
	v_cvt_pk_fp8_f32 v52, v56, v57
	v_mul_f32_e32 v53, 0x42800000, v53
	v_med3_f32 v56, v60, s50, v51
	v_med3_f32 v53, v53, s50, v51
	v_cvt_pk_fp8_f32 v52, v56, v53 op_sel:[0,0,1]
	s_waitcnt lgkmcnt(1)
	v_mul_f32_e32 v53, 0x42800000, v54
	v_mul_f32_e32 v54, 0x42800000, v55
	v_med3_f32 v56, v53, s50, v51
	v_med3_f32 v54, v54, s50, v51
	v_mov_b32_e32 v53, v3
	v_cvt_pk_fp8_f32 v53, v56, v54
	s_waitcnt lgkmcnt(0)
	v_mul_f32_e32 v55, 0x42800000, v58
	v_mul_f32_e32 v54, 0x42800000, v59
	v_med3_f32 v55, v55, s50, v51
	v_med3_f32 v54, v54, s50, v51
	v_cvt_pk_fp8_f32 v53, v55, v54 op_sel:[0,0,1]
	v_or_b32_e32 v54, s8, v15
	v_mov_b32_e32 v55, v3
	v_lshlrev_b64 v[54:55], 10, v[54:55]
	ds_read2_b32 v[56:57], v27 offset1:1
	v_lshl_add_u64 v[54:55], v[10:11], 0, v[54:55]
	global_store_dwordx2 v[54:55], v[52:53], off nt
	ds_read2_b32 v[52:53], v28 offset1:1
	ds_read2_b32 v[54:55], v29 offset1:1
	ds_read2_b32 v[58:59], v30 offset1:1
	s_waitcnt lgkmcnt(3)
	v_mul_f32_e32 v56, 0x42800000, v56
	v_mul_f32_e32 v57, 0x42800000, v57
	s_waitcnt lgkmcnt(2)
	v_mul_f32_e32 v60, 0x42800000, v52
	v_med3_f32 v56, v56, s50, v51
	v_med3_f32 v57, v57, s50, v51
	v_mov_b32_e32 v52, v3
	v_cvt_pk_fp8_f32 v52, v56, v57
	v_mul_f32_e32 v53, 0x42800000, v53
	v_med3_f32 v56, v60, s50, v51
	v_med3_f32 v53, v53, s50, v51
	v_cvt_pk_fp8_f32 v52, v56, v53 op_sel:[0,0,1]
	s_waitcnt lgkmcnt(1)
	v_mul_f32_e32 v53, 0x42800000, v54
	v_mul_f32_e32 v54, 0x42800000, v55
	v_med3_f32 v56, v53, s50, v51
	v_med3_f32 v54, v54, s50, v51
	v_mov_b32_e32 v53, v3
	v_cvt_pk_fp8_f32 v53, v56, v54
	s_waitcnt lgkmcnt(0)
	v_mul_f32_e32 v55, 0x42800000, v58
	v_mul_f32_e32 v54, 0x42800000, v59
	v_med3_f32 v55, v55, s50, v51
	v_med3_f32 v54, v54, s50, v51
	v_cvt_pk_fp8_f32 v53, v55, v54 op_sel:[0,0,1]
	v_or_b32_e32 v54, s8, v16
	v_mov_b32_e32 v55, v3
	v_lshlrev_b64 v[54:55], 10, v[54:55]
	ds_read2_b32 v[56:57], v31 offset1:1
	v_lshl_add_u64 v[54:55], v[10:11], 0, v[54:55]
	global_store_dwordx2 v[54:55], v[52:53], off nt
	ds_read2_b32 v[52:53], v32 offset1:1
	ds_read2_b32 v[54:55], v33 offset1:1
	ds_read2_b32 v[58:59], v34 offset1:1
	s_waitcnt lgkmcnt(3)
	v_mul_f32_e32 v56, 0x42800000, v56
	v_mul_f32_e32 v57, 0x42800000, v57
	s_waitcnt lgkmcnt(2)
	v_mul_f32_e32 v60, 0x42800000, v52
	v_med3_f32 v56, v56, s50, v51
	v_med3_f32 v57, v57, s50, v51
	v_mov_b32_e32 v52, v3
	v_cvt_pk_fp8_f32 v52, v56, v57
	v_mul_f32_e32 v53, 0x42800000, v53
	v_med3_f32 v56, v60, s50, v51
	v_med3_f32 v53, v53, s50, v51
	v_cvt_pk_fp8_f32 v52, v56, v53 op_sel:[0,0,1]
	s_waitcnt lgkmcnt(1)
	v_mul_f32_e32 v53, 0x42800000, v54
	v_mul_f32_e32 v54, 0x42800000, v55
	v_med3_f32 v56, v53, s50, v51
	v_med3_f32 v54, v54, s50, v51
	v_mov_b32_e32 v53, v3
	v_cvt_pk_fp8_f32 v53, v56, v54
	s_waitcnt lgkmcnt(0)
	v_mul_f32_e32 v55, 0x42800000, v58
	v_mul_f32_e32 v54, 0x42800000, v59
	v_med3_f32 v55, v55, s50, v51
	v_med3_f32 v54, v54, s50, v51
	v_cvt_pk_fp8_f32 v53, v55, v54 op_sel:[0,0,1]
	v_or_b32_e32 v54, s8, v17
	v_mov_b32_e32 v55, v3
	v_lshlrev_b64 v[54:55], 10, v[54:55]
	ds_read2_b32 v[56:57], v35 offset1:1
	v_lshl_add_u64 v[54:55], v[10:11], 0, v[54:55]
	global_store_dwordx2 v[54:55], v[52:53], off nt
	ds_read2_b32 v[52:53], v36 offset1:1
	ds_read2_b32 v[54:55], v37 offset1:1
	ds_read2_b32 v[58:59], v38 offset1:1
	s_waitcnt lgkmcnt(3)
	v_mul_f32_e32 v56, 0x42800000, v56
	v_mul_f32_e32 v57, 0x42800000, v57
	s_waitcnt lgkmcnt(2)
	v_mul_f32_e32 v60, 0x42800000, v52
	v_med3_f32 v56, v56, s50, v51
	v_med3_f32 v57, v57, s50, v51
	v_mov_b32_e32 v52, v3
	v_cvt_pk_fp8_f32 v52, v56, v57
	v_mul_f32_e32 v53, 0x42800000, v53
	v_med3_f32 v56, v60, s50, v51
	v_med3_f32 v53, v53, s50, v51
	v_cvt_pk_fp8_f32 v52, v56, v53 op_sel:[0,0,1]
	s_waitcnt lgkmcnt(1)
	v_mul_f32_e32 v53, 0x42800000, v54
	v_mul_f32_e32 v54, 0x42800000, v55
	v_med3_f32 v56, v53, s50, v51
	v_med3_f32 v54, v54, s50, v51
	v_mov_b32_e32 v53, v3
	v_cvt_pk_fp8_f32 v53, v56, v54
	s_waitcnt lgkmcnt(0)
	v_mul_f32_e32 v55, 0x42800000, v58
	v_mul_f32_e32 v54, 0x42800000, v59
	v_med3_f32 v55, v55, s50, v51
	v_med3_f32 v54, v54, s50, v51
	v_cvt_pk_fp8_f32 v53, v55, v54 op_sel:[0,0,1]
	v_or_b32_e32 v54, s8, v18
	v_mov_b32_e32 v55, v3
	v_lshlrev_b64 v[54:55], 10, v[54:55]
	ds_read2_b32 v[56:57], v39 offset1:1
	v_lshl_add_u64 v[54:55], v[10:11], 0, v[54:55]
	global_store_dwordx2 v[54:55], v[52:53], off nt
	ds_read2_b32 v[52:53], v40 offset1:1
	ds_read2_b32 v[54:55], v41 offset1:1
	ds_read2_b32 v[58:59], v42 offset1:1
	s_waitcnt lgkmcnt(3)
	v_mul_f32_e32 v56, 0x42800000, v56
	v_mul_f32_e32 v57, 0x42800000, v57
	s_waitcnt lgkmcnt(2)
	v_mul_f32_e32 v60, 0x42800000, v52
	v_med3_f32 v56, v56, s50, v51
	v_med3_f32 v57, v57, s50, v51
	v_mov_b32_e32 v52, v3
	v_cvt_pk_fp8_f32 v52, v56, v57
	v_mul_f32_e32 v53, 0x42800000, v53
	v_med3_f32 v56, v60, s50, v51
	v_med3_f32 v53, v53, s50, v51
	v_cvt_pk_fp8_f32 v52, v56, v53 op_sel:[0,0,1]
	s_waitcnt lgkmcnt(1)
	v_mul_f32_e32 v53, 0x42800000, v54
	v_mul_f32_e32 v54, 0x42800000, v55
	v_med3_f32 v56, v53, s50, v51
	v_med3_f32 v54, v54, s50, v51
	v_mov_b32_e32 v53, v3
	v_cvt_pk_fp8_f32 v53, v56, v54
	s_waitcnt lgkmcnt(0)
	v_mul_f32_e32 v55, 0x42800000, v58
	v_mul_f32_e32 v54, 0x42800000, v59
	v_med3_f32 v55, v55, s50, v51
	v_med3_f32 v54, v54, s50, v51
	v_cvt_pk_fp8_f32 v53, v55, v54 op_sel:[0,0,1]
	v_or_b32_e32 v54, s8, v19
	v_mov_b32_e32 v55, v3
	v_lshlrev_b64 v[54:55], 10, v[54:55]
	ds_read2_b32 v[56:57], v43 offset1:1
	v_lshl_add_u64 v[54:55], v[10:11], 0, v[54:55]
	global_store_dwordx2 v[54:55], v[52:53], off nt
	ds_read2_b32 v[52:53], v44 offset1:1
	ds_read2_b32 v[54:55], v45 offset1:1
	ds_read2_b32 v[58:59], v46 offset1:1
	s_waitcnt lgkmcnt(3)
	v_mul_f32_e32 v56, 0x42800000, v56
	v_mul_f32_e32 v57, 0x42800000, v57
	s_waitcnt lgkmcnt(2)
	v_mul_f32_e32 v60, 0x42800000, v52
	v_med3_f32 v56, v56, s50, v51
	v_med3_f32 v57, v57, s50, v51
	v_mov_b32_e32 v52, v3
	v_cvt_pk_fp8_f32 v52, v56, v57
	v_mul_f32_e32 v53, 0x42800000, v53
	v_med3_f32 v56, v60, s50, v51
	v_med3_f32 v53, v53, s50, v51
	v_cvt_pk_fp8_f32 v52, v56, v53 op_sel:[0,0,1]
	s_waitcnt lgkmcnt(1)
	v_mul_f32_e32 v53, 0x42800000, v54
	v_mul_f32_e32 v54, 0x42800000, v55
	v_med3_f32 v56, v53, s50, v51
	v_med3_f32 v54, v54, s50, v51
	v_mov_b32_e32 v53, v3
	v_cvt_pk_fp8_f32 v53, v56, v54
	s_waitcnt lgkmcnt(0)
	v_mul_f32_e32 v55, 0x42800000, v58
	v_mul_f32_e32 v54, 0x42800000, v59
	v_med3_f32 v55, v55, s50, v51
	v_med3_f32 v54, v54, s50, v51
	v_cvt_pk_fp8_f32 v53, v55, v54 op_sel:[0,0,1]
	v_or_b32_e32 v54, s8, v20
	v_mov_b32_e32 v55, v3
	v_lshlrev_b64 v[54:55], 10, v[54:55]
	ds_read2_b32 v[56:57], v47 offset1:1
	v_lshl_add_u64 v[54:55], v[10:11], 0, v[54:55]
	global_store_dwordx2 v[54:55], v[52:53], off nt
	ds_read2_b32 v[52:53], v48 offset1:1
	ds_read2_b32 v[54:55], v49 offset1:1
	ds_read2_b32 v[58:59], v50 offset1:1
	s_waitcnt lgkmcnt(3)
	v_mul_f32_e32 v56, 0x42800000, v56
	v_mul_f32_e32 v57, 0x42800000, v57
	s_waitcnt lgkmcnt(2)
	v_mul_f32_e32 v60, 0x42800000, v52
	v_med3_f32 v56, v56, s50, v51
	v_med3_f32 v57, v57, s50, v51
	v_mov_b32_e32 v52, v3
	v_cvt_pk_fp8_f32 v52, v56, v57
	v_mul_f32_e32 v53, 0x42800000, v53
	v_med3_f32 v56, v60, s50, v51
	v_med3_f32 v53, v53, s50, v51
	v_cvt_pk_fp8_f32 v52, v56, v53 op_sel:[0,0,1]
	s_waitcnt lgkmcnt(1)
	v_mul_f32_e32 v53, 0x42800000, v54
	v_mul_f32_e32 v54, 0x42800000, v55
	v_med3_f32 v56, v53, s50, v51
	v_med3_f32 v54, v54, s50, v51
	v_mov_b32_e32 v53, v3
	v_cvt_pk_fp8_f32 v53, v56, v54
	s_waitcnt lgkmcnt(0)
	v_mul_f32_e32 v55, 0x42800000, v58
	v_mul_f32_e32 v54, 0x42800000, v59
	v_med3_f32 v55, v55, s50, v51
	v_med3_f32 v54, v54, s50, v51
	v_cvt_pk_fp8_f32 v53, v55, v54 op_sel:[0,0,1]
	v_or_b32_e32 v54, s8, v21
	v_mov_b32_e32 v55, v3
	v_lshlrev_b64 v[54:55], 10, v[54:55]
	v_lshl_add_u64 v[10:11], v[10:11], 0, v[54:55]
	global_store_dwordx2 v[10:11], v[52:53], off nt
	s_waitcnt lgkmcnt(0)

.LBB0_62:
	s_andn2_b64 vcc, exec, s[14:15]
	s_cbranch_vccnz .LBB0_39
	s_mul_hi_i32 s8, s12, 0x780000
	s_mul_i32 s12, s12, 0x780000
	s_add_u32 s40, s26, s12
	s_addc_u32 s8, s27, s8
	s_bfe_u32 s12, s90, 0x4001b
	s_add_i32 s12, s90, s12
	s_sext_i32_i16 s13, s12
	s_and_b32 s12, s12, 0xfff0
	s_sub_i32 s12, s90, s12
	s_sext_i32_i16 s12, s12
	s_lshl_b32 s42, s12, 6
	s_lshl_b32 s12, s13, 2
	s_andn2_b32 s12, s12, 63
	s_ashr_i32 s13, s12, 31
	s_lshl_b64 s[14:15], s[12:13], 2
	v_or_b32_e32 v52, s42, v9
	s_add_u32 s14, s88, s14
	s_addc_u32 s15, s89, s15
	v_mul_i32_i24_e32 v52, 0x1300, v52
	v_lshl_add_u64 v[10:11], s[14:15], 0, v[2:3]
	v_ashrrev_i32_e32 v53, 31, v52
	v_lshl_add_u64 v[10:11], v[52:53], 2, v[10:11]
	v_add_co_u32_e32 v56, vcc, s68, v10
	s_ashr_i32 s13, s42, 31
	s_nop 0
	v_addc_co_u32_e32 v57, vcc, 0, v11, vcc
	v_add_co_u32_e32 v60, vcc, s69, v10
	global_load_dwordx4 v[52:55], v[10:11], off nt
	s_nop 0
	global_load_dwordx4 v[56:59], v[56:57], off nt
	v_addc_co_u32_e32 v61, vcc, 0, v11, vcc
	v_add_co_u32_e32 v64, vcc, s70, v10
	s_add_u32 s14, s40, s42
	s_nop 0
	v_addc_co_u32_e32 v65, vcc, 0, v11, vcc
	v_add_co_u32_e32 v68, vcc, s71, v10
	global_load_dwordx4 v[60:63], v[60:61], off nt
	s_nop 0
	global_load_dwordx4 v[64:67], v[64:65], off nt
	v_addc_co_u32_e32 v69, vcc, 0, v11, vcc
	v_add_co_u32_e32 v72, vcc, s72, v10
	s_addc_u32 s15, s8, s13
	s_nop 0
	v_addc_co_u32_e32 v73, vcc, 0, v11, vcc
	v_add_co_u32_e32 v76, vcc, s73, v10
	global_load_dwordx4 v[68:71], v[68:69], off nt
	s_nop 0
	global_load_dwordx4 v[72:75], v[72:73], off nt
	v_addc_co_u32_e32 v77, vcc, 0, v11, vcc
	v_add_co_u32_e32 v80, vcc, s74, v10
	s_nop 1
	v_addc_co_u32_e32 v81, vcc, 0, v11, vcc
	v_add_co_u32_e32 v84, vcc, s75, v10
	global_load_dwordx4 v[76:79], v[76:77], off nt
	s_nop 0
	global_load_dwordx4 v[80:83], v[80:81], off nt
	v_addc_co_u32_e32 v85, vcc, 0, v11, vcc
	v_add_co_u32_e32 v88, vcc, s76, v10
	s_nop 1
	v_addc_co_u32_e32 v89, vcc, 0, v11, vcc
	v_add_co_u32_e32 v92, vcc, s77, v10
	s_nop 1
	v_addc_co_u32_e32 v93, vcc, 0, v11, vcc
	v_add_co_u32_e32 v96, vcc, s78, v10
	s_nop 1
	v_addc_co_u32_e32 v97, vcc, 0, v11, vcc
	v_add_co_u32_e32 v100, vcc, s79, v10
	global_load_dwordx4 v[84:87], v[84:85], off nt
	s_nop 0
	global_load_dwordx4 v[88:91], v[88:89], off nt
	s_nop 0
	global_load_dwordx4 v[92:95], v[92:93], off nt
	s_nop 0
	global_load_dwordx4 v[96:99], v[96:97], off nt
	v_addc_co_u32_e32 v101, vcc, 0, v11, vcc
	v_add_co_u32_e32 v104, vcc, s80, v10
	s_nop 1
	v_addc_co_u32_e32 v105, vcc, 0, v11, vcc
	v_add_co_u32_e32 v108, vcc, s81, v10
	global_load_dwordx4 v[100:103], v[100:101], off nt
	s_nop 0
	global_load_dwordx4 v[104:107], v[104:105], off nt
	v_addc_co_u32_e32 v109, vcc, 0, v11, vcc
	v_add_co_u32_e32 v10, vcc, s82, v10
	s_nop 1
	v_addc_co_u32_e32 v11, vcc, 0, v11, vcc
	global_load_dwordx4 v[108:111], v[108:109], off nt
	s_nop 0
	global_load_dwordx4 v[112:115], v[10:11], off nt
	v_lshl_add_u64 v[10:11], s[14:15], 0, v[4:5]
	s_waitcnt vmcnt(14)
	ds_write2_b32 v12, v52, v56 offset1:4
	ds_write2_b32 v12, v53, v57 offset0:65 offset1:69
	ds_write2_b32 v12, v54, v58 offset0:130 offset1:134
	ds_write2_b32 v12, v55, v59 offset0:195 offset1:199
	s_waitcnt vmcnt(12)
	ds_write2_b32 v12, v60, v64 offset0:8 offset1:12
	ds_write2_b32 v12, v61, v65 offset0:73 offset1:77
	ds_write2_b32 v12, v62, v66 offset0:138 offset1:142
	ds_write2_b32 v12, v63, v67 offset0:203 offset1:207
	s_waitcnt vmcnt(10)
	ds_write2_b32 v12, v68, v72 offset0:16 offset1:20
	ds_write2_b32 v12, v69, v73 offset0:81 offset1:85
	ds_write2_b32 v12, v70, v74 offset0:146 offset1:150
	ds_write2_b32 v12, v71, v75 offset0:211 offset1:215
	s_waitcnt vmcnt(8)
	ds_write2_b32 v12, v76, v80 offset0:24 offset1:28
	ds_write2_b32 v12, v77, v81 offset0:89 offset1:93
	ds_write2_b32 v12, v78, v82 offset0:154 offset1:158
	ds_write2_b32 v12, v79, v83 offset0:219 offset1:223
	s_waitcnt vmcnt(6)
	ds_write2_b32 v12, v84, v88 offset0:32 offset1:36
	ds_write2_b32 v12, v85, v89 offset0:97 offset1:101
	ds_write2_b32 v12, v86, v90 offset0:162 offset1:166
	ds_write2_b32 v12, v87, v91 offset0:227 offset1:231
	s_waitcnt vmcnt(4)
	ds_write2_b32 v12, v92, v96 offset0:40 offset1:44
	ds_write2_b32 v12, v93, v97 offset0:105 offset1:109
	ds_write2_b32 v12, v94, v98 offset0:170 offset1:174
	ds_write2_b32 v12, v95, v99 offset0:235 offset1:239
	s_waitcnt vmcnt(2)
	ds_write2_b32 v12, v100, v104 offset0:48 offset1:52
	ds_write2_b32 v12, v101, v105 offset0:113 offset1:117
	ds_write2_b32 v12, v102, v106 offset0:178 offset1:182
	ds_write2_b32 v12, v103, v107 offset0:243 offset1:247
	s_waitcnt vmcnt(0)
	ds_write2_b32 v12, v108, v112 offset0:56 offset1:60
	ds_write2_b32 v12, v109, v113 offset0:121 offset1:125
	ds_write2_b32 v12, v110, v114 offset0:186 offset1:190
	ds_write2_b32 v12, v111, v115 offset0:251 offset1:255
	s_waitcnt lgkmcnt(0)
	ds_read2_b32 v[52:53], v14 offset1:1
	ds_read2_b32 v[54:55], v14 offset0:2 offset1:3
	ds_read2_b32 v[56:57], v14 offset0:4 offset1:5
	ds_read2_b32 v[58:59], v14 offset0:6 offset1:7
	s_waitcnt lgkmcnt(2)
	v_mul_f32_e32 v54, 0x42800000, v54
	v_mul_f32_e32 v52, 0x42800000, v52
	v_mul_f32_e32 v53, 0x42800000, v53
	v_med3_f32 v60, v52, s50, v51
	v_med3_f32 v53, v53, s50, v51
	v_mov_b32_e32 v52, v3
	v_cvt_pk_fp8_f32 v52, v60, v53
	v_mul_f32_e32 v53, 0x42800000, v55
	v_med3_f32 v54, v54, s50, v51
	v_med3_f32 v53, v53, s50, v51
	v_cvt_pk_fp8_f32 v52, v54, v53 op_sel:[0,0,1]
	s_waitcnt lgkmcnt(1)
	v_mul_f32_e32 v53, 0x42800000, v56
	v_mul_f32_e32 v54, 0x42800000, v57
	v_med3_f32 v56, v53, s50, v51
	v_med3_f32 v54, v54, s50, v51
	v_mov_b32_e32 v53, v3
	v_cvt_pk_fp8_f32 v53, v56, v54
	s_waitcnt lgkmcnt(0)
	v_mul_f32_e32 v55, 0x42800000, v58
	v_mul_f32_e32 v54, 0x42800000, v59
	v_med3_f32 v55, v55, s50, v51
	v_med3_f32 v54, v54, s50, v51
	v_cvt_pk_fp8_f32 v53, v55, v54 op_sel:[0,0,1]
	v_or_b32_e32 v54, s12, v13
	v_ashrrev_i32_e32 v55, 31, v54
	v_lshlrev_b64 v[54:55], 10, v[54:55]
	ds_read2_b32 v[56:57], v26 offset1:1
	v_lshl_add_u64 v[54:55], v[10:11], 0, v[54:55]
	global_store_dwordx2 v[54:55], v[52:53], off nt
	ds_read2_b32 v[52:53], v26 offset0:2 offset1:3
	ds_read2_b32 v[54:55], v26 offset0:4 offset1:5
	ds_read2_b32 v[58:59], v26 offset0:6 offset1:7
	s_waitcnt lgkmcnt(3)
	v_mul_f32_e32 v56, 0x42800000, v56
	v_mul_f32_e32 v57, 0x42800000, v57
	s_waitcnt lgkmcnt(2)
	v_mul_f32_e32 v60, 0x42800000, v52
	v_med3_f32 v56, v56, s50, v51
	v_med3_f32 v57, v57, s50, v51
	v_mov_b32_e32 v52, v3
	v_cvt_pk_fp8_f32 v52, v56, v57
	v_mul_f32_e32 v53, 0x42800000, v53
	v_med3_f32 v56, v60, s50, v51
	v_med3_f32 v53, v53, s50, v51
	v_cvt_pk_fp8_f32 v52, v56, v53 op_sel:[0,0,1]
	s_waitcnt lgkmcnt(1)
	v_mul_f32_e32 v53, 0x42800000, v54
	v_mul_f32_e32 v54, 0x42800000, v55
	v_med3_f32 v56, v53, s50, v51
	v_med3_f32 v54, v54, s50, v51
	v_mov_b32_e32 v53, v3
	v_cvt_pk_fp8_f32 v53, v56, v54
	s_waitcnt lgkmcnt(0)
	v_mul_f32_e32 v55, 0x42800000, v58
	v_mul_f32_e32 v54, 0x42800000, v59
	v_med3_f32 v55, v55, s50, v51
	v_med3_f32 v54, v54, s50, v51
	v_cvt_pk_fp8_f32 v53, v55, v54 op_sel:[0,0,1]
	v_or_b32_e32 v54, s12, v15
	v_ashrrev_i32_e32 v55, 31, v54
	v_lshlrev_b64 v[54:55], 10, v[54:55]
	ds_read2_b32 v[56:57], v27 offset1:1
	v_lshl_add_u64 v[54:55], v[10:11], 0, v[54:55]
	global_store_dwordx2 v[54:55], v[52:53], off nt
	ds_read2_b32 v[52:53], v28 offset1:1
	ds_read2_b32 v[54:55], v29 offset1:1
	ds_read2_b32 v[58:59], v30 offset1:1
	s_waitcnt lgkmcnt(3)
	v_mul_f32_e32 v56, 0x42800000, v56
	v_mul_f32_e32 v57, 0x42800000, v57
	s_waitcnt lgkmcnt(2)
	v_mul_f32_e32 v60, 0x42800000, v52
	v_med3_f32 v56, v56, s50, v51
	v_med3_f32 v57, v57, s50, v51
	v_mov_b32_e32 v52, v3
	v_cvt_pk_fp8_f32 v52, v56, v57
	v_mul_f32_e32 v53, 0x42800000, v53
	v_med3_f32 v56, v60, s50, v51
	v_med3_f32 v53, v53, s50, v51
	v_cvt_pk_fp8_f32 v52, v56, v53 op_sel:[0,0,1]
	s_waitcnt lgkmcnt(1)
	v_mul_f32_e32 v53, 0x42800000, v54
	v_mul_f32_e32 v54, 0x42800000, v55
	v_med3_f32 v56, v53, s50, v51
	v_med3_f32 v54, v54, s50, v51
	v_mov_b32_e32 v53, v3
	v_cvt_pk_fp8_f32 v53, v56, v54
	s_waitcnt lgkmcnt(0)
	v_mul_f32_e32 v55, 0x42800000, v58
	v_mul_f32_e32 v54, 0x42800000, v59
	v_med3_f32 v55, v55, s50, v51
	v_med3_f32 v54, v54, s50, v51
	v_cvt_pk_fp8_f32 v53, v55, v54 op_sel:[0,0,1]
	v_or_b32_e32 v54, s12, v16
	v_ashrrev_i32_e32 v55, 31, v54
	v_lshlrev_b64 v[54:55], 10, v[54:55]
	ds_read2_b32 v[56:57], v31 offset1:1
	v_lshl_add_u64 v[54:55], v[10:11], 0, v[54:55]
	global_store_dwordx2 v[54:55], v[52:53], off nt
	ds_read2_b32 v[52:53], v32 offset1:1
	ds_read2_b32 v[54:55], v33 offset1:1
	ds_read2_b32 v[58:59], v34 offset1:1
	s_waitcnt lgkmcnt(3)
	v_mul_f32_e32 v56, 0x42800000, v56
	v_mul_f32_e32 v57, 0x42800000, v57
	s_waitcnt lgkmcnt(2)
	v_mul_f32_e32 v60, 0x42800000, v52
	v_med3_f32 v56, v56, s50, v51
	v_med3_f32 v57, v57, s50, v51
	v_mov_b32_e32 v52, v3
	v_cvt_pk_fp8_f32 v52, v56, v57
	v_mul_f32_e32 v53, 0x42800000, v53
	v_med3_f32 v56, v60, s50, v51
	v_med3_f32 v53, v53, s50, v51
	v_cvt_pk_fp8_f32 v52, v56, v53 op_sel:[0,0,1]
	s_waitcnt lgkmcnt(1)
	v_mul_f32_e32 v53, 0x42800000, v54
	v_mul_f32_e32 v54, 0x42800000, v55
	v_med3_f32 v56, v53, s50, v51
	v_med3_f32 v54, v54, s50, v51
	v_mov_b32_e32 v53, v3
	v_cvt_pk_fp8_f32 v53, v56, v54
	s_waitcnt lgkmcnt(0)
	v_mul_f32_e32 v55, 0x42800000, v58
	v_mul_f32_e32 v54, 0x42800000, v59
	v_med3_f32 v55, v55, s50, v51
	v_med3_f32 v54, v54, s50, v51
	v_cvt_pk_fp8_f32 v53, v55, v54 op_sel:[0,0,1]
	v_or_b32_e32 v54, s12, v17
	v_ashrrev_i32_e32 v55, 31, v54
	v_lshlrev_b64 v[54:55], 10, v[54:55]
	ds_read2_b32 v[56:57], v35 offset1:1
	v_lshl_add_u64 v[54:55], v[10:11], 0, v[54:55]
	global_store_dwordx2 v[54:55], v[52:53], off nt
	ds_read2_b32 v[52:53], v36 offset1:1
	ds_read2_b32 v[54:55], v37 offset1:1
	ds_read2_b32 v[58:59], v38 offset1:1
	s_waitcnt lgkmcnt(3)
	v_mul_f32_e32 v56, 0x42800000, v56
	v_mul_f32_e32 v57, 0x42800000, v57
	s_waitcnt lgkmcnt(2)
	v_mul_f32_e32 v60, 0x42800000, v52
	v_med3_f32 v56, v56, s50, v51
	v_med3_f32 v57, v57, s50, v51
	v_mov_b32_e32 v52, v3
	v_cvt_pk_fp8_f32 v52, v56, v57
	v_mul_f32_e32 v53, 0x42800000, v53
	v_med3_f32 v56, v60, s50, v51
	v_med3_f32 v53, v53, s50, v51
	v_cvt_pk_fp8_f32 v52, v56, v53 op_sel:[0,0,1]
	s_waitcnt lgkmcnt(1)
	v_mul_f32_e32 v53, 0x42800000, v54
	v_mul_f32_e32 v54, 0x42800000, v55
	v_med3_f32 v56, v53, s50, v51
	v_med3_f32 v54, v54, s50, v51
	v_mov_b32_e32 v53, v3
	v_cvt_pk_fp8_f32 v53, v56, v54
	s_waitcnt lgkmcnt(0)
	v_mul_f32_e32 v55, 0x42800000, v58
	v_mul_f32_e32 v54, 0x42800000, v59
	v_med3_f32 v55, v55, s50, v51
	v_med3_f32 v54, v54, s50, v51
	v_cvt_pk_fp8_f32 v53, v55, v54 op_sel:[0,0,1]
	v_or_b32_e32 v54, s12, v18
	v_ashrrev_i32_e32 v55, 31, v54
	v_lshlrev_b64 v[54:55], 10, v[54:55]
	ds_read2_b32 v[56:57], v39 offset1:1
	v_lshl_add_u64 v[54:55], v[10:11], 0, v[54:55]
	global_store_dwordx2 v[54:55], v[52:53], off nt
	ds_read2_b32 v[52:53], v40 offset1:1
	ds_read2_b32 v[54:55], v41 offset1:1
	ds_read2_b32 v[58:59], v42 offset1:1
	s_waitcnt lgkmcnt(3)
	v_mul_f32_e32 v56, 0x42800000, v56
	v_mul_f32_e32 v57, 0x42800000, v57
	s_waitcnt lgkmcnt(2)
	v_mul_f32_e32 v60, 0x42800000, v52
	v_med3_f32 v56, v56, s50, v51
	v_med3_f32 v57, v57, s50, v51
	v_mov_b32_e32 v52, v3
	v_cvt_pk_fp8_f32 v52, v56, v57
	v_mul_f32_e32 v53, 0x42800000, v53
	v_med3_f32 v56, v60, s50, v51
	v_med3_f32 v53, v53, s50, v51
	v_cvt_pk_fp8_f32 v52, v56, v53 op_sel:[0,0,1]
	s_waitcnt lgkmcnt(1)
	v_mul_f32_e32 v53, 0x42800000, v54
	v_mul_f32_e32 v54, 0x42800000, v55
	v_med3_f32 v56, v53, s50, v51
	v_med3_f32 v54, v54, s50, v51
	v_mov_b32_e32 v53, v3
	v_cvt_pk_fp8_f32 v53, v56, v54
	s_waitcnt lgkmcnt(0)
	v_mul_f32_e32 v55, 0x42800000, v58
	v_mul_f32_e32 v54, 0x42800000, v59
	v_med3_f32 v55, v55, s50, v51
	v_med3_f32 v54, v54, s50, v51
	v_cvt_pk_fp8_f32 v53, v55, v54 op_sel:[0,0,1]
	v_or_b32_e32 v54, s12, v19
	v_ashrrev_i32_e32 v55, 31, v54
	v_lshlrev_b64 v[54:55], 10, v[54:55]
	ds_read2_b32 v[56:57], v43 offset1:1
	v_lshl_add_u64 v[54:55], v[10:11], 0, v[54:55]
	global_store_dwordx2 v[54:55], v[52:53], off nt
	ds_read2_b32 v[52:53], v44 offset1:1
	ds_read2_b32 v[54:55], v45 offset1:1
	ds_read2_b32 v[58:59], v46 offset1:1
	s_waitcnt lgkmcnt(3)
	v_mul_f32_e32 v56, 0x42800000, v56
	v_mul_f32_e32 v57, 0x42800000, v57
	s_waitcnt lgkmcnt(2)
	v_mul_f32_e32 v60, 0x42800000, v52
	v_med3_f32 v56, v56, s50, v51
	v_med3_f32 v57, v57, s50, v51
	v_mov_b32_e32 v52, v3
	v_cvt_pk_fp8_f32 v52, v56, v57
	v_mul_f32_e32 v53, 0x42800000, v53
	v_med3_f32 v56, v60, s50, v51
	v_med3_f32 v53, v53, s50, v51
	v_cvt_pk_fp8_f32 v52, v56, v53 op_sel:[0,0,1]
	s_waitcnt lgkmcnt(1)
	v_mul_f32_e32 v53, 0x42800000, v54
	v_mul_f32_e32 v54, 0x42800000, v55
	v_med3_f32 v56, v53, s50, v51
	v_med3_f32 v54, v54, s50, v51
	v_mov_b32_e32 v53, v3
	v_cvt_pk_fp8_f32 v53, v56, v54
	s_waitcnt lgkmcnt(0)
	v_mul_f32_e32 v55, 0x42800000, v58
	v_mul_f32_e32 v54, 0x42800000, v59
	v_med3_f32 v55, v55, s50, v51
	v_med3_f32 v54, v54, s50, v51
	v_cvt_pk_fp8_f32 v53, v55, v54 op_sel:[0,0,1]
	v_or_b32_e32 v54, s12, v20
	v_ashrrev_i32_e32 v55, 31, v54
	v_lshlrev_b64 v[54:55], 10, v[54:55]
	ds_read2_b32 v[56:57], v47 offset1:1
	v_lshl_add_u64 v[54:55], v[10:11], 0, v[54:55]
	global_store_dwordx2 v[54:55], v[52:53], off nt
	ds_read2_b32 v[52:53], v48 offset1:1
	ds_read2_b32 v[54:55], v49 offset1:1
	ds_read2_b32 v[58:59], v50 offset1:1
	s_waitcnt lgkmcnt(3)
	v_mul_f32_e32 v56, 0x42800000, v56
	v_mul_f32_e32 v57, 0x42800000, v57
	s_waitcnt lgkmcnt(2)
	v_mul_f32_e32 v60, 0x42800000, v52
	v_med3_f32 v56, v56, s50, v51
	v_med3_f32 v57, v57, s50, v51
	v_mov_b32_e32 v52, v3
	v_cvt_pk_fp8_f32 v52, v56, v57
	v_mul_f32_e32 v53, 0x42800000, v53
	v_med3_f32 v56, v60, s50, v51
	v_med3_f32 v53, v53, s50, v51
	v_cvt_pk_fp8_f32 v52, v56, v53 op_sel:[0,0,1]
	s_waitcnt lgkmcnt(1)
	v_mul_f32_e32 v53, 0x42800000, v54
	v_mul_f32_e32 v54, 0x42800000, v55
	v_med3_f32 v56, v53, s50, v51
	v_med3_f32 v54, v54, s50, v51
	v_mov_b32_e32 v53, v3
	v_cvt_pk_fp8_f32 v53, v56, v54
	s_waitcnt lgkmcnt(0)
	v_mul_f32_e32 v55, 0x42800000, v58
	v_mul_f32_e32 v54, 0x42800000, v59
	v_med3_f32 v55, v55, s50, v51
	v_med3_f32 v54, v54, s50, v51
	v_cvt_pk_fp8_f32 v53, v55, v54 op_sel:[0,0,1]
	v_or_b32_e32 v54, s12, v21
	v_ashrrev_i32_e32 v55, 31, v54
	v_lshlrev_b64 v[54:55], 10, v[54:55]
	v_lshl_add_u64 v[10:11], v[10:11], 0, v[54:55]
	global_store_dwordx2 v[10:11], v[52:53], off nt
	s_waitcnt lgkmcnt(0)
	s_branch .LBB0_39

.LBB0_334:
	s_ff1_i32_b32 s29, s34
	v_readlane_b32 s35, v37, s29
	s_add_i32 s33, s34, -1
	v_readlane_b32 s36, v39, s29
	s_mulk_i32 s29, 0x1200
	s_ashr_i32 s37, s35, 31
	v_mul_f32_e32 v72, s36, v208
	s_add_u32 s36, s35, s29
	s_addc_u32 s37, s37, 0
	s_lshl_b64 s[36:37], s[36:37], 10
	v_lshl_add_u64 v[102:103], v[28:29], 0, s[36:37]
	global_load_dword v100, v[102:103], off nt
	global_load_dword v99, v[102:103], off offset:256 nt
	global_load_dword v98, v[102:103], off offset:512 nt
	global_load_dword v94, v[102:103], off offset:768 nt
	s_and_b32 s29, s33, s34

.LBB0_336:
	s_cmp_eq_u32 s29, 0
	s_mov_b32 s33, 0
	v_mov_b32_e32 v43, 0
	v_mov_b32_e32 v45, 0
	v_mov_b32_e32 v47, 0
	v_mov_b32_e32 v49, 0
	v_mov_b32_e32 v42, 0
	s_mov_b32 s34, 0
	s_cbranch_scc1 .LBB0_338
	s_ff1_i32_b32 s34, s29
	v_readlane_b32 s35, v37, s34
	v_readlane_b32 s37, v39, s34
	s_add_i32 s36, s29, -1
	s_mulk_i32 s34, 0x1200
	v_mul_f32_e32 v42, s37, v208
	s_ashr_i32 s37, s35, 31
	s_add_u32 s34, s35, s34
	s_addc_u32 s35, s37, 0
	s_lshl_b64 s[34:35], s[34:35], 10
	v_lshl_add_u64 v[60:61], v[28:29], 0, s[34:35]
	global_load_dword v49, v[60:61], off nt
	global_load_dword v47, v[60:61], off offset:256 nt
	global_load_dword v45, v[60:61], off offset:512 nt
	global_load_dword v43, v[60:61], off offset:768 nt
	s_and_b32 s34, s36, s29
.LBB0_338:
	v_mov_b32_e32 v69, 0
	s_cmp_eq_u32 s34, 0
	v_mov_b32_e32 v61, 0
	v_mov_b32_e32 v71, 0
	v_mov_b32_e32 v76, 0
	v_mov_b32_e32 v77, 0
	v_mov_b32_e32 v44, 0
	s_cbranch_scc1 .LBB0_340
	s_ff1_i32_b32 s29, s34
	v_readlane_b32 s35, v37, s29
	s_add_i32 s33, s34, -1
	v_readlane_b32 s36, v39, s29
	s_mulk_i32 s29, 0x1200
	s_ashr_i32 s37, s35, 31
	v_mul_f32_e32 v44, s36, v208
	s_add_u32 s36, s35, s29
	s_addc_u32 s37, s37, 0
	s_lshl_b64 s[36:37], s[36:37], 10
	v_lshl_add_u64 v[68:69], v[28:29], 0, s[36:37]
	global_load_dword v77, v[68:69], off nt
	global_load_dword v76, v[68:69], off offset:256 nt
	global_load_dword v71, v[68:69], off offset:512 nt
	s_nop 0
	global_load_dword v69, v[68:69], off offset:768 nt
	s_and_b32 s33, s33, s34
.LBB0_340:
	s_cmp_eq_u32 s33, 0
	s_mov_b32 s29, 0
	v_mov_b32_e32 v78, 0
	v_mov_b32_e32 v79, 0
	v_mov_b32_e32 v80, 0
	v_mov_b32_e32 v46, 0
	s_mov_b32 s34, 0
	s_cbranch_scc1 .LBB0_342
	s_ff1_i32_b32 s36, s33
	v_readlane_b32 s34, v37, s36
	s_add_i32 s37, s33, -1
	s_mul_i32 s35, s36, 0x1200
	s_ashr_i32 s38, s34, 31
	s_add_u32 s34, s34, s35
	s_addc_u32 s35, s38, 0
	s_lshl_b64 s[34:35], s[34:35], 10
	v_lshl_add_u64 v[60:61], v[28:29], 0, s[34:35]
	global_load_dword v80, v[60:61], off nt
	global_load_dword v79, v[60:61], off offset:256 nt
	global_load_dword v78, v[60:61], off offset:512 nt
	s_nop 0
	global_load_dword v61, v[60:61], off offset:768 nt
	v_readlane_b32 s34, v39, s36
	s_nop 1
	v_mul_f32_e32 v46, s34, v208
	s_and_b32 s34, s37, s33
.LBB0_342:
	v_mov_b32_e32 v82, 0
	s_cmp_eq_u32 s34, 0
	v_mov_b32_e32 v81, 0
	v_mov_b32_e32 v83, 0
	v_mov_b32_e32 v84, 0
	v_mov_b32_e32 v85, 0
	v_mov_b32_e32 v48, 0
	s_cbranch_scc1 .LBB0_344
	s_ff1_i32_b32 s29, s34
	v_readlane_b32 s35, v37, s29
	s_add_i32 s33, s34, -1
	v_readlane_b32 s36, v39, s29
	s_mulk_i32 s29, 0x1200
	s_ashr_i32 s37, s35, 31
	v_mul_f32_e32 v48, s36, v208
	s_add_u32 s36, s35, s29
	s_addc_u32 s37, s37, 0
	s_lshl_b64 s[36:37], s[36:37], 10
	v_lshl_add_u64 v[86:87], v[28:29], 0, s[36:37]
	global_load_dword v85, v[86:87], off nt
	global_load_dword v84, v[86:87], off offset:256 nt
	global_load_dword v83, v[86:87], off offset:512 nt
	global_load_dword v82, v[86:87], off offset:768 nt
	s_and_b32 s29, s33, s34
.LBB0_344:
	s_cmp_eq_u32 s29, 0
	s_mov_b32 s33, 0
	v_mov_b32_e32 v86, 0
	v_mov_b32_e32 v87, 0
	v_mov_b32_e32 v88, 0
	v_mov_b32_e32 v60, 0
	s_mov_b32 s34, 0
	s_cbranch_scc1 .LBB0_346
	s_ff1_i32_b32 s34, s29
	v_readlane_b32 s35, v37, s34
	v_readlane_b32 s37, v39, s34
	s_add_i32 s36, s29, -1
	s_mulk_i32 s34, 0x1200
	v_mul_f32_e32 v60, s37, v208
	s_ashr_i32 s37, s35, 31
	s_add_u32 s34, s35, s34
	s_addc_u32 s35, s37, 0
	s_lshl_b64 s[34:35], s[34:35], 10
	v_lshl_add_u64 v[90:91], v[28:29], 0, s[34:35]
	global_load_dword v88, v[90:91], off nt
	global_load_dword v87, v[90:91], off offset:256 nt
	global_load_dword v86, v[90:91], off offset:512 nt
	global_load_dword v81, v[90:91], off offset:768 nt
	s_and_b32 s34, s36, s29
.LBB0_346:
	v_mov_b32_e32 v90, 0
	s_cmp_eq_u32 s34, 0
	v_mov_b32_e32 v89, 0
	v_mov_b32_e32 v91, 0
	v_mov_b32_e32 v92, 0
	v_mov_b32_e32 v93, 0
	v_mov_b32_e32 v68, 0
	s_cbranch_scc1 .LBB0_348
	s_ff1_i32_b32 s29, s34
	v_readlane_b32 s35, v37, s29
	s_add_i32 s33, s34, -1
	v_readlane_b32 s36, v39, s29
	s_mulk_i32 s29, 0x1200
	s_ashr_i32 s37, s35, 31
	v_mul_f32_e32 v68, s36, v208
	s_add_u32 s36, s35, s29
	s_addc_u32 s37, s37, 0
	s_lshl_b64 s[36:37], s[36:37], 10
	v_lshl_add_u64 v[94:95], v[28:29], 0, s[36:37]
	global_load_dword v93, v[94:95], off nt
	global_load_dword v92, v[94:95], off offset:256 nt
	global_load_dword v91, v[94:95], off offset:512 nt
	global_load_dword v90, v[94:95], off offset:768 nt
	s_and_b32 s33, s33, s34
.LBB0_348:
	s_cmp_eq_u32 s33, 0
	s_mov_b32 s29, 0
	v_mov_b32_e32 v95, 0
	v_mov_b32_e32 v96, 0
	v_mov_b32_e32 v97, 0
	v_mov_b32_e32 v70, 0
	s_mov_b32 s34, 0
	s_cbranch_scc1 .LBB0_350
	s_ff1_i32_b32 s34, s33
	v_readlane_b32 s35, v37, s34
	v_readlane_b32 s37, v39, s34
	s_add_i32 s36, s33, -1
	s_mulk_i32 s34, 0x1200
	v_mul_f32_e32 v70, s37, v208
	s_ashr_i32 s37, s35, 31
	s_add_u32 s34, s35, s34
	s_addc_u32 s35, s37, 0
	s_lshl_b64 s[34:35], s[34:35], 10
	v_lshl_add_u64 v[98:99], v[28:29], 0, s[34:35]
	global_load_dword v97, v[98:99], off nt
	global_load_dword v96, v[98:99], off offset:256 nt
	global_load_dword v95, v[98:99], off offset:512 nt
	global_load_dword v89, v[98:99], off offset:768 nt
	s_and_b32 s34, s36, s33
